# hoist gain loads out of store loops in L0 rows_norm, L1 rows_moe, p9 scatter x2
# baseline (speedup 1.0000x reference)
.LBB0_113:
	s_andn2_b64 vcc, exec, s[0:1]
	s_mul_i32 s82, s90, 24
	s_cbranch_vccnz .LBB0_171
	s_and_b64 vcc, exec, s[4:5]
	s_cbranch_vccnz .LBB0_171
	v_mov_b32_e32 v133, 0
	v_lshlrev_b32_e32 v2, 2, v130
	v_lshlrev_b32_e32 v146, 3, v130
	v_mov_b32_e32 v147, v133
	v_xor_b32_e32 v1, 64, v2
	v_xor_b32_e32 v131, 0x80, v2
	v_lshl_add_u64 v[2:3], s[12:13], 0, v[146:147]
	s_mov_b64 s[0:1], 0x16400000
	v_lshl_add_u64 v[148:149], v[2:3], 0, s[0:1]
	s_add_i32 s0, s10, s94
	s_ashr_i32 s1, s0, 31
	s_lshl_b32 s14, s90, 5
	s_lshl_b32 s33, s90, 4
	s_lshl_b64 s[4:5], s[0:1], 12
	s_add_u32 s16, s12, s4
	s_addc_u32 s17, s13, s5
	s_ashr_i32 s15, s14, 31
	s_lshl_b64 s[18:19], s[14:15], 12
	s_lshl_b64 s[0:1], s[0:1], 13
	v_readlane_b32 s36, v233, 0
	v_readlane_b32 s37, v233, 1
	s_add_u32 s20, s36, s0
	v_lshlrev_b32_e32 v134, 4, v130
	s_addc_u32 s21, s37, s1
	s_ashr_i32 s11, s10, 31
	v_or_b32_e32 v132, 0x1000, v134
	s_lshl_b64 s[22:23], s[14:15], 13
	s_lshl_b64 s[0:1], s[10:11], 13
	v_lshl_add_u64 v[138:139], s[8:9], 0, v[132:133]
	v_or_b32_e32 v132, 0x1400, v134
	s_add_u32 s24, s36, s0
	v_lshl_add_u64 v[140:141], s[8:9], 0, v[132:133]
	v_or_b32_e32 v132, 0x1800, v134
	s_addc_u32 s25, s37, s1
	s_lshl_b64 s[0:1], s[10:11], 12
	v_mov_b32_e32 v135, v133
	v_lshl_add_u64 v[142:143], s[8:9], 0, v[132:133]
	v_or_b32_e32 v132, 0x1c00, v134
	s_add_u32 s12, s12, s0
	v_lshl_add_u64 v[136:137], s[8:9], 0, v[134:135]
	v_lshl_add_u64 v[144:145], s[8:9], 0, v[132:133]
	s_addc_u32 s13, s13, s1
	v_mov_b32_e32 v152, 0x358637bd
	s_mov_b32 s11, 0xf800000
	v_mov_b32_e32 v153, 0x260
	s_movk_i32 s15, 0x7fff
	s_mov_b32 s34, 0x16400000
	v_mov_b32_e32 v154, 1
	v_readlane_b32 s38, v233, 2
	v_readlane_b32 s39, v233, 3
	v_readlane_b32 s40, v233, 4
	v_readlane_b32 s41, v233, 5
	v_readlane_b32 s42, v233, 6
	v_readlane_b32 s43, v233, 7
	v_readlane_b32 s44, v233, 8
	v_readlane_b32 s45, v233, 9
	v_readlane_b32 s46, v233, 10
	v_readlane_b32 s47, v233, 11
	v_readlane_b32 s48, v233, 12
	v_readlane_b32 s49, v233, 13
	v_readlane_b32 s50, v233, 14
	v_readlane_b32 s51, v233, 15
	global_load_dwordx4 v[166:169], v[136:137], off
	global_load_dwordx4 v[170:173], v[136:137], off offset:1024
	global_load_dwordx4 v[174:177], v[136:137], off offset:2048
	global_load_dwordx4 v[178:181], v[136:137], off offset:3072
	global_load_dwordx4 v[182:185], v[138:139], off
	global_load_dwordx4 v[186:189], v[140:141], off
	global_load_dwordx4 v[190:193], v[142:143], off
	global_load_dwordx4 v[194:197], v[144:145], off
	s_waitcnt vmcnt(0)
	s_branch .LBB0_117

.LBB0_165:
	s_waitcnt vmcnt(7)
	v_mov_b32_e32 v156, v127
	s_waitcnt vmcnt(6)
	v_mov_b32_e32 v157, v123
	v_mov_b32_e32 v150, v126
	v_mov_b32_e32 v151, v122
	v_pk_mul_f32 v[156:157], v[156:157], v[156:157]
	v_mov_b32_e32 v158, v129
	v_mov_b32_e32 v159, v125
	v_pk_fma_f32 v[150:151], v[150:151], v[150:151], v[156:157]
	v_mov_b32_e32 v156, v128
	v_mov_b32_e32 v157, v124
	v_pk_mul_f32 v[158:159], v[158:159], v[158:159]
	s_waitcnt vmcnt(3)
	v_mul_f32_e32 v132, v110, v110
	v_pk_fma_f32 v[156:157], v[156:157], v[156:157], v[158:159]
	v_pk_mul_f32 v[158:159], v[118:119], v[118:119]
	v_pk_add_f32 v[150:151], v[150:151], v[156:157]
	v_pk_mul_f32 v[156:157], v[120:121], v[120:121]
	v_mul_f32_e32 v155, v111, v111
	v_pk_mov_b32 v[160:161], v[158:159], v[156:157] op_sel:[1,0]
	v_mov_b32_e32 v159, v157
	v_pk_add_f32 v[156:157], v[160:161], v[158:159]
	v_pk_add_f32 v[150:151], v[150:151], v[150:151] op_sel:[0,1] op_sel_hi:[1,0]
	v_pk_add_f32 v[156:157], v[156:157], v[156:157] op_sel:[0,1] op_sel_hi:[1,0]
	v_mov_b32_e32 v151, v132
	v_mov_b32_e32 v157, v155
	v_mul_f32_e32 v132, v115, v115
	v_mul_f32_e32 v158, v112, v112
	v_pk_add_f32 v[150:151], v[150:151], v[156:157]
	v_pk_fma_f32 v[156:157], v[114:115], v[114:115], v[132:133] op_sel_hi:[1,1,0]
	v_mul_f32_e32 v132, v117, v117
	v_mul_f32_e32 v160, v113, v113
	v_mov_b32_e32 v157, v158
	v_pk_fma_f32 v[158:159], v[116:117], v[116:117], v[132:133] op_sel_hi:[1,1,0]
	s_waitcnt vmcnt(2)
	v_pk_mul_f32 v[162:163], v[106:107], v[106:107]
	v_mov_b32_e32 v159, v160
	v_pk_add_f32 v[156:157], v[156:157], v[158:159]
	v_pk_mul_f32 v[160:161], v[108:109], v[108:109]
	v_pk_add_f32 v[150:151], v[150:151], v[156:157]
	v_mov_b64_e32 v[156:157], v[166:167]
	v_mov_b64_e32 v[158:159], v[168:169]
	v_pk_mov_b32 v[164:165], v[162:163], v[160:161] op_sel:[1,0]
	v_mov_b32_e32 v163, v161
	v_pk_add_f32 v[160:161], v[164:165], v[162:163]
	s_waitcnt vmcnt(0)
	v_mul_f32_e32 v132, v98, v98
	v_mul_f32_e32 v155, v99, v99
	v_pk_add_f32 v[150:151], v[150:151], v[150:151] op_sel:[0,1] op_sel_hi:[1,0]
	v_pk_add_f32 v[160:161], v[160:161], v[160:161] op_sel:[0,1] op_sel_hi:[1,0]
	v_mov_b32_e32 v151, v132
	v_mov_b32_e32 v161, v155
	v_mul_f32_e32 v132, v103, v103
	v_mul_f32_e32 v162, v100, v100
	v_pk_add_f32 v[150:151], v[150:151], v[160:161]
	v_pk_fma_f32 v[160:161], v[102:103], v[102:103], v[132:133] op_sel_hi:[1,1,0]
	v_mul_f32_e32 v132, v105, v105
	v_mul_f32_e32 v164, v101, v101
	v_mov_b32_e32 v161, v162
	v_pk_fma_f32 v[162:163], v[104:105], v[104:105], v[132:133] op_sel_hi:[1,1,0]
	s_nop 0
	v_mov_b32_e32 v163, v164
	v_pk_add_f32 v[160:161], v[160:161], v[162:163]
	v_mul_f32_e32 v162, v45, v45
	v_pk_add_f32 v[150:151], v[150:151], v[160:161]
	v_fmac_f32_e32 v162, v44, v44
	v_add_f32_e32 v132, v150, v151
	v_mul_f32_e32 v163, v35, v35
	v_mul_f32_e32 v164, v37, v37
	v_add_f32_dpp v132, v132, v132 quad_perm:[1,0,3,2] row_mask:0xf bank_mask:0xf bound_ctrl:1
	v_fmac_f32_e32 v163, v34, v34
	v_fmac_f32_e32 v164, v36, v36
	v_add_f32_dpp v132, v132, v132 quad_perm:[2,3,0,1] row_mask:0xf bank_mask:0xf bound_ctrl:1
	s_nop 1
	v_add_f32_dpp v132, v132, v132 row_ror:4 row_mask:0xf bank_mask:0xf bound_ctrl:1
	s_nop 1
	v_add_f32_dpp v132, v132, v132 row_ror:8 row_mask:0xf bank_mask:0xf bound_ctrl:1
	ds_bpermute_b32 v150, v1, v132
	s_waitcnt lgkmcnt(0)
	v_add_f32_e32 v132, v132, v150
	ds_bpermute_b32 v150, v131, v132
	s_waitcnt lgkmcnt(0)
	v_add_f32_e32 v132, v132, v150
	v_fmamk_f32 v132, v132, 0x3a000000, v152
	v_cmp_gt_f32_e32 vcc, s11, v132
	v_mul_f32_e32 v150, 0x4f800000, v132
	s_nop 0
	v_cndmask_b32_e32 v132, v132, v150, vcc
	v_sqrt_f32_e32 v150, v132
	s_nop 0
	v_add_u32_e32 v151, -1, v150
	v_fma_f32 v155, -v151, v150, v132
	v_cmp_ge_f32_e64 s[0:1], 0, v155
	v_add_u32_e32 v155, 1, v150
	s_nop 0
	v_cndmask_b32_e64 v151, v150, v151, s[0:1]
	v_fma_f32 v150, -v155, v150, v132
	v_cmp_lt_f32_e64 s[0:1], 0, v150
	s_nop 1
	v_cndmask_b32_e64 v150, v151, v155, s[0:1]
	v_mul_f32_e32 v151, 0x37800000, v150
	v_cndmask_b32_e32 v150, v150, v151, vcc
	v_cmp_class_f32_e32 vcc, v132, v153
	s_nop 1
	v_cndmask_b32_e32 v132, v150, v132, vcc
	v_div_scale_f32 v150, s[0:1], v132, v132, 1.0
	v_rcp_f32_e32 v151, v150
	s_nop 0
	v_fma_f32 v155, -v150, v151, 1.0
	v_fmac_f32_e32 v151, v155, v151
	v_div_scale_f32 v155, vcc, 1.0, v132, 1.0
	v_mul_f32_e32 v160, v155, v151
	v_fma_f32 v161, -v150, v160, v155
	v_fmac_f32_e32 v160, v161, v151
	v_fma_f32 v150, -v150, v160, v155
	v_div_fmas_f32 v150, v150, v151, v160
	v_div_fixup_f32 v132, v150, v132, 1.0
	v_mov_b32_e32 v150, v126
	v_mov_b32_e32 v151, v128
	v_pk_mul_f32 v[150:151], v[150:151], v[132:133] op_sel_hi:[1,0]
	v_mov_b32_e32 v160, v156
	v_mov_b32_e32 v161, v158
	v_mov_b32_e32 v128, v127
	v_pk_mul_f32 v[150:151], v[160:161], v[150:151]
	v_pk_mul_f32 v[126:127], v[128:129], v[132:133] op_sel_hi:[1,0]
	v_mov_b32_e32 v158, v157
	v_pk_mul_f32 v[126:127], v[158:159], v[126:127]
	v_and_b32_sdwa v128, v151, v154 dst_sel:DWORD dst_unused:UNUSED_PAD src0_sel:WORD_1 src1_sel:DWORD
	v_and_b32_sdwa v129, v150, v154 dst_sel:DWORD dst_unused:UNUSED_PAD src0_sel:WORD_1 src1_sel:DWORD
	v_add3_u32 v150, v150, v129, s15
	v_add3_u32 v128, v151, v128, s15
	v_and_b32_sdwa v129, v127, v154 dst_sel:DWORD dst_unused:UNUSED_PAD src0_sel:WORD_1 src1_sel:DWORD
	v_and_b32_sdwa v151, v126, v154 dst_sel:DWORD dst_unused:UNUSED_PAD src0_sel:WORD_1 src1_sel:DWORD
	v_add3_u32 v127, v127, v129, s15
	v_add3_u32 v126, v126, v151, s15
	v_and_b32_e32 v127, 0xffff0000, v127
	v_and_b32_e32 v126, 0xffff0000, v126
	v_or_b32_sdwa v129, v127, v128 dst_sel:DWORD dst_unused:UNUSED_PAD src0_sel:DWORD src1_sel:WORD_1
	v_or_b32_sdwa v128, v126, v150 dst_sel:DWORD dst_unused:UNUSED_PAD src0_sel:DWORD src1_sel:WORD_1
	v_lshl_add_u64 v[126:127], s[12:13], 0, v[146:147]
	v_add_co_u32_e32 v126, vcc, s34, v126
	v_mul_f32_e32 v155, v63, v63
	s_nop 0
	v_addc_co_u32_e32 v127, vcc, 0, v127, vcc
	global_store_dwordx2 v[126:127], v[128:129], off
	v_mov_b64_e32 v[156:157], v[170:171]
	v_mov_b64_e32 v[158:159], v[172:173]
	v_mov_b32_e32 v128, v122
	v_mov_b32_e32 v129, v124
	v_mov_b32_e32 v124, v123
	v_pk_mul_f32 v[122:123], v[128:129], v[132:133] op_sel_hi:[1,0]
	v_pk_mul_f32 v[124:125], v[124:125], v[132:133] op_sel_hi:[1,0]
	v_fmac_f32_e32 v155, v62, v62
	v_mul_f32_e32 v160, v61, v61
	v_mul_f32_e32 v161, v43, v43
	v_fmac_f32_e32 v160, v60, v60
	v_fmac_f32_e32 v161, v42, v42
	s_and_b64 vcc, exec, s[8:9]
	v_mov_b32_e32 v129, v158
	v_mov_b32_e32 v158, v157
	v_mov_b32_e32 v128, v156
	v_pk_mul_f32 v[124:125], v[158:159], v[124:125]
	v_pk_mul_f32 v[122:123], v[128:129], v[122:123]
	v_and_b32_sdwa v150, v125, v154 dst_sel:DWORD dst_unused:UNUSED_PAD src0_sel:WORD_1 src1_sel:DWORD
	v_and_b32_sdwa v151, v124, v154 dst_sel:DWORD dst_unused:UNUSED_PAD src0_sel:WORD_1 src1_sel:DWORD
	v_and_b32_sdwa v128, v123, v154 dst_sel:DWORD dst_unused:UNUSED_PAD src0_sel:WORD_1 src1_sel:DWORD
	v_and_b32_sdwa v129, v122, v154 dst_sel:DWORD dst_unused:UNUSED_PAD src0_sel:WORD_1 src1_sel:DWORD
	v_add3_u32 v125, v125, v150, s15
	v_add3_u32 v124, v124, v151, s15
	v_add3_u32 v122, v122, v129, s15
	v_add3_u32 v123, v123, v128, s15
	v_and_b32_e32 v125, 0xffff0000, v125
	v_and_b32_e32 v124, 0xffff0000, v124
	v_or_b32_sdwa v123, v125, v123 dst_sel:DWORD dst_unused:UNUSED_PAD src0_sel:DWORD src1_sel:WORD_1
	v_or_b32_sdwa v122, v124, v122 dst_sel:DWORD dst_unused:UNUSED_PAD src0_sel:DWORD src1_sel:WORD_1
	global_store_dwordx2 v[126:127], v[122:123], off offset:512
	v_mov_b64_e32 v[122:123], v[174:175]
	v_mov_b64_e32 v[124:125], v[176:177]
	v_mov_b32_e32 v128, v118
	v_mov_b32_e32 v129, v120
	v_mov_b32_e32 v120, v119
	v_pk_mul_f32 v[118:119], v[128:129], v[132:133] op_sel_hi:[1,0]
	v_pk_mul_f32 v[120:121], v[120:121], v[132:133] op_sel_hi:[1,0]
	v_mul_f32_e32 v150, v39, v39
	v_mul_f32_e32 v151, v41, v41
	v_mul_f32_e32 v156, v65, v65
	v_mul_f32_e32 v157, v51, v51
	v_mul_f32_e32 v158, v53, v53
	v_fmac_f32_e32 v150, v38, v38
	v_fmac_f32_e32 v151, v40, v40
	v_fmac_f32_e32 v156, v64, v64
	v_mul_f32_e32 v159, v59, v59
	v_fmac_f32_e32 v157, v50, v50
	v_fmac_f32_e32 v158, v52, v52
	v_fmac_f32_e32 v159, v58, v58
	v_mov_b32_e32 v129, v124
	v_mov_b32_e32 v124, v123
	v_mov_b32_e32 v128, v122
	v_pk_mul_f32 v[120:121], v[120:121], v[124:125]
	v_pk_mul_f32 v[118:119], v[118:119], v[128:129]
	v_and_b32_sdwa v124, v121, v154 dst_sel:DWORD dst_unused:UNUSED_PAD src0_sel:WORD_1 src1_sel:DWORD
	v_and_b32_sdwa v125, v120, v154 dst_sel:DWORD dst_unused:UNUSED_PAD src0_sel:WORD_1 src1_sel:DWORD
	v_and_b32_sdwa v122, v119, v154 dst_sel:DWORD dst_unused:UNUSED_PAD src0_sel:WORD_1 src1_sel:DWORD
	v_and_b32_sdwa v123, v118, v154 dst_sel:DWORD dst_unused:UNUSED_PAD src0_sel:WORD_1 src1_sel:DWORD
	v_add3_u32 v121, v121, v124, s15
	v_add3_u32 v120, v120, v125, s15
	v_add3_u32 v118, v118, v123, s15
	v_add3_u32 v119, v119, v122, s15
	v_and_b32_e32 v121, 0xffff0000, v121
	v_and_b32_e32 v120, 0xffff0000, v120
	v_or_b32_sdwa v119, v121, v119 dst_sel:DWORD dst_unused:UNUSED_PAD src0_sel:DWORD src1_sel:WORD_1
	v_or_b32_sdwa v118, v120, v118 dst_sel:DWORD dst_unused:UNUSED_PAD src0_sel:DWORD src1_sel:WORD_1
	global_store_dwordx2 v[126:127], v[118:119], off offset:1024
	v_mov_b64_e32 v[118:119], v[178:179]
	v_mov_b64_e32 v[120:121], v[180:181]
	v_mov_b32_e32 v122, v114
	v_mov_b32_e32 v123, v116
	v_mov_b32_e32 v116, v115
	v_pk_mul_f32 v[114:115], v[122:123], v[132:133] op_sel_hi:[1,0]
	v_pk_mul_f32 v[116:117], v[116:117], v[132:133] op_sel_hi:[1,0]
	v_mul_f32_e32 v124, v67, v67
	v_mul_f32_e32 v125, v69, v69
	v_mul_f32_e32 v128, v75, v75
	v_mul_f32_e32 v129, v77, v77
	v_fmac_f32_e32 v124, v66, v66
	v_fmac_f32_e32 v125, v68, v68
	v_fmac_f32_e32 v128, v74, v74
	v_fmac_f32_e32 v129, v76, v76
	v_mov_b32_e32 v123, v120
	v_mov_b32_e32 v120, v119
	v_mov_b32_e32 v122, v118
	v_pk_mul_f32 v[116:117], v[116:117], v[120:121]
	v_pk_mul_f32 v[114:115], v[114:115], v[122:123]
	v_and_b32_sdwa v120, v117, v154 dst_sel:DWORD dst_unused:UNUSED_PAD src0_sel:WORD_1 src1_sel:DWORD
	v_and_b32_sdwa v121, v116, v154 dst_sel:DWORD dst_unused:UNUSED_PAD src0_sel:WORD_1 src1_sel:DWORD
	v_and_b32_sdwa v118, v115, v154 dst_sel:DWORD dst_unused:UNUSED_PAD src0_sel:WORD_1 src1_sel:DWORD
	v_and_b32_sdwa v119, v114, v154 dst_sel:DWORD dst_unused:UNUSED_PAD src0_sel:WORD_1 src1_sel:DWORD
	v_add3_u32 v117, v117, v120, s15
	v_add3_u32 v116, v116, v121, s15
	v_add3_u32 v114, v114, v119, s15
	v_add3_u32 v115, v115, v118, s15
	v_and_b32_e32 v117, 0xffff0000, v117
	v_and_b32_e32 v116, 0xffff0000, v116
	v_or_b32_sdwa v115, v117, v115 dst_sel:DWORD dst_unused:UNUSED_PAD src0_sel:DWORD src1_sel:WORD_1
	v_or_b32_sdwa v114, v116, v114 dst_sel:DWORD dst_unused:UNUSED_PAD src0_sel:DWORD src1_sel:WORD_1
	global_store_dwordx2 v[126:127], v[114:115], off offset:1536
	v_mov_b64_e32 v[114:115], v[182:183]
	v_mov_b64_e32 v[116:117], v[184:185]
	v_mov_b32_e32 v118, v110
	v_mov_b32_e32 v119, v112
	v_mov_b32_e32 v112, v111
	v_pk_mul_f32 v[110:111], v[118:119], v[132:133] op_sel_hi:[1,0]
	v_pk_mul_f32 v[112:113], v[112:113], v[132:133] op_sel_hi:[1,0]
	v_mul_f32_e32 v120, v71, v71
	v_mul_f32_e32 v121, v73, v73
	v_mul_f32_e32 v122, v83, v83
	v_mul_f32_e32 v123, v85, v85
	v_fmac_f32_e32 v120, v70, v70
	v_fmac_f32_e32 v121, v72, v72
	v_fmac_f32_e32 v122, v82, v82
	v_fmac_f32_e32 v123, v84, v84
	v_mov_b32_e32 v119, v116
	v_mov_b32_e32 v116, v115
	v_mov_b32_e32 v118, v114
	v_pk_mul_f32 v[112:113], v[112:113], v[116:117]
	v_pk_mul_f32 v[110:111], v[110:111], v[118:119]
	v_and_b32_sdwa v116, v113, v154 dst_sel:DWORD dst_unused:UNUSED_PAD src0_sel:WORD_1 src1_sel:DWORD
	v_and_b32_sdwa v117, v112, v154 dst_sel:DWORD dst_unused:UNUSED_PAD src0_sel:WORD_1 src1_sel:DWORD
	v_and_b32_sdwa v114, v111, v154 dst_sel:DWORD dst_unused:UNUSED_PAD src0_sel:WORD_1 src1_sel:DWORD
	v_and_b32_sdwa v115, v110, v154 dst_sel:DWORD dst_unused:UNUSED_PAD src0_sel:WORD_1 src1_sel:DWORD
	v_add3_u32 v113, v113, v116, s15
	v_add3_u32 v112, v112, v117, s15
	v_add3_u32 v110, v110, v115, s15
	v_add3_u32 v111, v111, v114, s15
	v_and_b32_e32 v113, 0xffff0000, v113
	v_and_b32_e32 v112, 0xffff0000, v112
	v_or_b32_sdwa v111, v113, v111 dst_sel:DWORD dst_unused:UNUSED_PAD src0_sel:DWORD src1_sel:WORD_1
	v_or_b32_sdwa v110, v112, v110 dst_sel:DWORD dst_unused:UNUSED_PAD src0_sel:DWORD src1_sel:WORD_1
	global_store_dwordx2 v[126:127], v[110:111], off offset:2048
	v_mov_b64_e32 v[110:111], v[186:187]
	v_mov_b64_e32 v[112:113], v[188:189]
	v_mov_b32_e32 v114, v106
	v_mov_b32_e32 v115, v108
	v_mov_b32_e32 v108, v107
	v_pk_mul_f32 v[106:107], v[114:115], v[132:133] op_sel_hi:[1,0]
	v_pk_mul_f32 v[108:109], v[108:109], v[132:133] op_sel_hi:[1,0]
	v_mul_f32_e32 v116, v79, v79
	v_mul_f32_e32 v117, v81, v81
	v_mul_f32_e32 v118, v87, v87
	v_mul_f32_e32 v119, v89, v89
	v_fmac_f32_e32 v116, v78, v78
	v_fmac_f32_e32 v117, v80, v80
	v_fmac_f32_e32 v118, v86, v86
	v_fmac_f32_e32 v119, v88, v88
	v_mov_b32_e32 v115, v112
	v_mov_b32_e32 v112, v111
	v_mov_b32_e32 v114, v110
	v_pk_mul_f32 v[108:109], v[108:109], v[112:113]
	v_pk_mul_f32 v[106:107], v[106:107], v[114:115]
	v_and_b32_sdwa v112, v109, v154 dst_sel:DWORD dst_unused:UNUSED_PAD src0_sel:WORD_1 src1_sel:DWORD
	v_and_b32_sdwa v113, v108, v154 dst_sel:DWORD dst_unused:UNUSED_PAD src0_sel:WORD_1 src1_sel:DWORD
	v_and_b32_sdwa v110, v107, v154 dst_sel:DWORD dst_unused:UNUSED_PAD src0_sel:WORD_1 src1_sel:DWORD
	v_and_b32_sdwa v111, v106, v154 dst_sel:DWORD dst_unused:UNUSED_PAD src0_sel:WORD_1 src1_sel:DWORD
	v_add3_u32 v109, v109, v112, s15
	v_add3_u32 v108, v108, v113, s15
	v_add3_u32 v106, v106, v111, s15
	v_add3_u32 v107, v107, v110, s15
	v_and_b32_e32 v109, 0xffff0000, v109
	v_and_b32_e32 v108, 0xffff0000, v108
	v_or_b32_sdwa v107, v109, v107 dst_sel:DWORD dst_unused:UNUSED_PAD src0_sel:DWORD src1_sel:WORD_1
	v_or_b32_sdwa v106, v108, v106 dst_sel:DWORD dst_unused:UNUSED_PAD src0_sel:DWORD src1_sel:WORD_1
	global_store_dwordx2 v[126:127], v[106:107], off offset:2560
	v_mov_b64_e32 v[106:107], v[190:191]
	v_mov_b64_e32 v[108:109], v[192:193]
	v_mov_b32_e32 v110, v102
	v_mov_b32_e32 v111, v104
	v_mov_b32_e32 v104, v103
	v_pk_mul_f32 v[102:103], v[104:105], v[132:133] op_sel_hi:[1,0]
	v_mul_f32_e32 v112, v95, v95
	v_mul_f32_e32 v113, v97, v97
	v_mul_f32_e32 v114, v91, v91
	v_mul_f32_e32 v115, v93, v93
	v_fmac_f32_e32 v112, v94, v94
	v_fmac_f32_e32 v113, v96, v96
	v_fmac_f32_e32 v114, v90, v90
	v_fmac_f32_e32 v115, v92, v92
	v_mov_b32_e32 v104, v106
	v_mov_b32_e32 v105, v108
	v_mov_b32_e32 v108, v107
	v_pk_mul_f32 v[106:107], v[110:111], v[132:133] op_sel_hi:[1,0]
	v_pk_mul_f32 v[102:103], v[102:103], v[108:109]
	v_pk_mul_f32 v[104:105], v[106:107], v[104:105]
	v_add_f32_e32 v111, v112, v113
	v_and_b32_sdwa v106, v105, v154 dst_sel:DWORD dst_unused:UNUSED_PAD src0_sel:WORD_1 src1_sel:DWORD
	v_and_b32_sdwa v107, v104, v154 dst_sel:DWORD dst_unused:UNUSED_PAD src0_sel:WORD_1 src1_sel:DWORD
	v_add3_u32 v104, v104, v107, s15
	v_add3_u32 v105, v105, v106, s15
	v_and_b32_sdwa v106, v103, v154 dst_sel:DWORD dst_unused:UNUSED_PAD src0_sel:WORD_1 src1_sel:DWORD
	v_and_b32_sdwa v107, v102, v154 dst_sel:DWORD dst_unused:UNUSED_PAD src0_sel:WORD_1 src1_sel:DWORD
	v_add3_u32 v103, v103, v106, s15
	v_add3_u32 v102, v102, v107, s15
	v_and_b32_e32 v103, 0xffff0000, v103
	v_and_b32_e32 v102, 0xffff0000, v102
	v_or_b32_sdwa v103, v103, v105 dst_sel:DWORD dst_unused:UNUSED_PAD src0_sel:DWORD src1_sel:WORD_1
	v_or_b32_sdwa v102, v102, v104 dst_sel:DWORD dst_unused:UNUSED_PAD src0_sel:DWORD src1_sel:WORD_1
	global_store_dwordx2 v[126:127], v[102:103], off offset:3072
	v_mov_b64_e32 v[102:103], v[194:195]
	v_mov_b64_e32 v[104:105], v[196:197]
	v_mul_f32_e32 v110, v7, v7
	v_add_f32_e32 v112, v114, v115
	v_mul_f32_e32 v113, v9, v9
	v_add_f32_e32 v114, v116, v117
	v_mul_f32_e32 v115, v31, v31
	v_mul_f32_e32 v117, v33, v33
	v_add_f32_e32 v116, v118, v119
	v_add_f32_e32 v118, v120, v121
	v_mul_f32_e32 v119, v19, v19
	v_mul_f32_e32 v121, v21, v21
	v_fmac_f32_e32 v110, v6, v6
	v_fmac_f32_e32 v113, v8, v8
	v_fmac_f32_e32 v115, v30, v30
	v_fmac_f32_e32 v117, v32, v32
	v_add_f32_e32 v120, v122, v123
	v_add_f32_e32 v122, v124, v125
	v_mul_f32_e32 v123, v27, v27
	v_add_f32_e32 v124, v128, v129
	v_mul_f32_e32 v125, v29, v29
	v_add_f32_e32 v128, v150, v151
	v_add_f32_e32 v150, v155, v156
	v_add_f32_e32 v113, v110, v113
	v_add_f32_e32 v115, v115, v117
	v_fmac_f32_e32 v119, v18, v18
	v_fmac_f32_e32 v121, v20, v20
	v_mul_f32_e32 v108, v55, v55
	v_mul_f32_e32 v109, v57, v57
	v_mul_f32_e32 v129, v11, v11
	v_mul_f32_e32 v151, v13, v13
	v_add_f32_e32 v155, v157, v158
	v_mov_b32_e32 v110, v98
	v_fmac_f32_e32 v123, v26, v26
	v_fmac_f32_e32 v125, v28, v28
	v_add_f32_e32 v98, v119, v121
	v_add_f32_e32 v111, v111, v112
	v_add_f32_e32 v112, v128, v150
	v_add_f32_e32 v113, v113, v115
	v_mul_f32_e32 v106, v47, v47
	v_mul_f32_e32 v107, v49, v49
	v_mul_f32_e32 v156, v23, v23
	v_add_f32_e32 v157, v159, v160
	v_mul_f32_e32 v158, v25, v25
	v_fmac_f32_e32 v108, v54, v54
	v_fmac_f32_e32 v109, v56, v56
	v_fmac_f32_e32 v129, v10, v10
	v_fmac_f32_e32 v151, v12, v12
	v_add_f32_e32 v117, v123, v125
	v_add_f32_e32 v111, v111, v114
	v_add_f32_e32 v112, v112, v155
	v_add_f32_e32 v98, v113, v98
	v_add_f32_e32 v159, v161, v162
	v_mul_f32_e32 v160, v3, v3
	v_add_f32_e32 v108, v108, v109
	v_mul_f32_e32 v109, v5, v5
	v_fmac_f32_e32 v106, v46, v46
	v_fmac_f32_e32 v107, v48, v48
	v_fmac_f32_e32 v156, v22, v22
	v_fmac_f32_e32 v158, v24, v24
	v_add_f32_e32 v119, v129, v151
	v_add_f32_e32 v111, v111, v116
	v_add_f32_e32 v112, v112, v157
	v_add_f32_e32 v98, v98, v117
	v_mul_f32_e32 v162, v15, v15
	v_add_f32_e32 v106, v106, v107
	v_mul_f32_e32 v107, v17, v17
	v_fmac_f32_e32 v160, v2, v2
	v_fmac_f32_e32 v109, v4, v4
	v_add_f32_e32 v121, v156, v158
	v_add_f32_e32 v111, v111, v118
	v_add_f32_e32 v112, v112, v159
	v_add_f32_e32 v98, v98, v119
	v_add_f32_e32 v161, v163, v164
	v_fmac_f32_e32 v162, v14, v14
	v_fmac_f32_e32 v107, v16, v16
	v_add_f32_e32 v109, v160, v109
	v_add_f32_e32 v111, v111, v120
	v_add_f32_e32 v108, v112, v108
	v_add_f32_e32 v98, v98, v121
	v_add_f32_e32 v107, v162, v107
	v_add_f32_e32 v111, v111, v122
	v_add_f32_e32 v108, v108, v161
	v_add_f32_e32 v98, v98, v109
	v_add_f32_e32 v109, v111, v124
	v_add_f32_e32 v106, v108, v106
	v_add_f32_e32 v98, v98, v107
	v_add_f32_dpp v107, v109, v109 quad_perm:[1,0,3,2] row_mask:0xf bank_mask:0xf bound_ctrl:1
	v_add_f32_dpp v106, v106, v106 quad_perm:[1,0,3,2] row_mask:0xf bank_mask:0xf bound_ctrl:1
	v_add_f32_dpp v98, v98, v98 quad_perm:[1,0,3,2] row_mask:0xf bank_mask:0xf bound_ctrl:1
	v_add_f32_dpp v107, v107, v107 quad_perm:[2,3,0,1] row_mask:0xf bank_mask:0xf bound_ctrl:1
	v_add_f32_dpp v106, v106, v106 quad_perm:[2,3,0,1] row_mask:0xf bank_mask:0xf bound_ctrl:1
	v_add_f32_dpp v98, v98, v98 quad_perm:[2,3,0,1] row_mask:0xf bank_mask:0xf bound_ctrl:1
	v_add_f32_dpp v107, v107, v107 row_ror:4 row_mask:0xf bank_mask:0xf bound_ctrl:1
	v_add_f32_dpp v106, v106, v106 row_ror:4 row_mask:0xf bank_mask:0xf bound_ctrl:1
	v_add_f32_dpp v98, v98, v98 row_ror:4 row_mask:0xf bank_mask:0xf bound_ctrl:1
	v_add_f32_dpp v107, v107, v107 row_ror:8 row_mask:0xf bank_mask:0xf bound_ctrl:1
	v_add_f32_dpp v106, v106, v106 row_ror:8 row_mask:0xf bank_mask:0xf bound_ctrl:1
	v_add_f32_dpp v98, v98, v98 row_ror:8 row_mask:0xf bank_mask:0xf bound_ctrl:1
	ds_bpermute_b32 v108, v1, v107
	ds_bpermute_b32 v109, v1, v106
	ds_bpermute_b32 v112, v1, v98
	v_mov_b32_e32 v111, v100
	v_mov_b32_e32 v100, v99
	s_waitcnt lgkmcnt(2)
	v_add_f32_e32 v108, v107, v108
	s_waitcnt lgkmcnt(1)
	v_add_f32_e32 v106, v106, v109
	s_waitcnt lgkmcnt(0)
	v_add_f32_e32 v98, v98, v112
	v_pk_mul_f32 v[100:101], v[100:101], v[132:133] op_sel_hi:[1,0]
	v_mov_b32_e32 v113, v104
	v_mov_b32_e32 v104, v103
	ds_bpermute_b32 v109, v131, v108
	ds_bpermute_b32 v107, v131, v106
	ds_bpermute_b32 v99, v131, v98
	v_pk_mul_f32 v[110:111], v[110:111], v[132:133] op_sel_hi:[1,0]
	v_mov_b32_e32 v112, v102
	v_pk_mul_f32 v[100:101], v[100:101], v[104:105]
	v_pk_mul_f32 v[102:103], v[110:111], v[112:113]
	v_and_b32_sdwa v110, v101, v154 dst_sel:DWORD dst_unused:UNUSED_PAD src0_sel:WORD_1 src1_sel:DWORD
	v_and_b32_sdwa v111, v100, v154 dst_sel:DWORD dst_unused:UNUSED_PAD src0_sel:WORD_1 src1_sel:DWORD
	v_and_b32_sdwa v104, v103, v154 dst_sel:DWORD dst_unused:UNUSED_PAD src0_sel:WORD_1 src1_sel:DWORD
	v_and_b32_sdwa v105, v102, v154 dst_sel:DWORD dst_unused:UNUSED_PAD src0_sel:WORD_1 src1_sel:DWORD
	v_add3_u32 v101, v101, v110, s15
	v_add3_u32 v100, v100, v111, s15
	v_add3_u32 v102, v102, v105, s15
	v_add3_u32 v103, v103, v104, s15
	v_and_b32_e32 v101, 0xffff0000, v101
	v_and_b32_e32 v100, 0xffff0000, v100
	v_or_b32_sdwa v101, v101, v103 dst_sel:DWORD dst_unused:UNUSED_PAD src0_sel:DWORD src1_sel:WORD_1
	v_or_b32_sdwa v100, v100, v102 dst_sel:DWORD dst_unused:UNUSED_PAD src0_sel:DWORD src1_sel:WORD_1
	global_store_dwordx2 v[126:127], v[100:101], off offset:3584
	s_cbranch_vccz .LBB0_168
	s_and_b64 vcc, exec, s[6:7]
	s_cbranch_vccz .LBB0_169

.LBB0_168:
	v_mov_b64_e32 v[100:101], v[166:167]
	v_mov_b64_e32 v[102:103], v[168:169]
	s_waitcnt lgkmcnt(2)
	v_add_f32_e32 v105, v108, v109
	v_mov_b32_e32 v104, v94
	v_fmamk_f32 v94, v105, 0x3a000000, v152
	v_mul_f32_e32 v105, 0x4f800000, v94
	v_cmp_gt_f32_e32 vcc, s11, v94
	s_nop 1
	v_cndmask_b32_e32 v108, v94, v105, vcc
	v_sqrt_f32_e32 v109, v108
	v_mov_b32_e32 v105, v96
	v_mov_b32_e32 v96, v95
	v_lshl_add_u64 v[94:95], s[16:17], 0, v[146:147]
	v_add_u32_e32 v110, -1, v109
	v_add_u32_e32 v111, 1, v109
	v_fma_f32 v112, -v110, v109, v108
	v_fma_f32 v113, -v111, v109, v108
	v_cmp_ge_f32_e64 s[0:1], 0, v112
	s_nop 1
	v_cndmask_b32_e64 v109, v109, v110, s[0:1]
	v_cmp_lt_f32_e64 s[0:1], 0, v113
	s_nop 1
	v_cndmask_b32_e64 v109, v109, v111, s[0:1]
	v_mul_f32_e32 v110, 0x37800000, v109
	v_cndmask_b32_e32 v109, v109, v110, vcc
	v_cmp_class_f32_e32 vcc, v108, v153
	s_nop 1
	v_cndmask_b32_e32 v108, v109, v108, vcc
	v_div_scale_f32 v109, s[0:1], v108, v108, 1.0
	v_rcp_f32_e32 v110, v109
	v_add_co_u32_e32 v94, vcc, s34, v94
	v_fma_f32 v112, -v109, v110, 1.0
	s_nop 0
	v_addc_co_u32_e32 v95, vcc, 0, v95, vcc
	v_div_scale_f32 v111, vcc, 1.0, v108, 1.0
	v_fmac_f32_e32 v110, v112, v110
	v_mul_f32_e32 v112, v111, v110
	v_fma_f32 v113, -v109, v112, v111
	v_fmac_f32_e32 v112, v113, v110
	v_fma_f32 v109, -v109, v112, v111
	v_div_fmas_f32 v109, v109, v110, v112
	v_div_fixup_f32 v108, v109, v108, 1.0
	v_pk_mul_f32 v[96:97], v[96:97], v[108:109] op_sel_hi:[1,0]
	v_pk_mul_f32 v[104:105], v[104:105], v[108:109] op_sel_hi:[1,0]
	v_mov_b32_e32 v111, v102
	v_mov_b32_e32 v102, v101
	v_mov_b32_e32 v110, v100
	v_pk_mul_f32 v[96:97], v[96:97], v[102:103]
	v_pk_mul_f32 v[100:101], v[104:105], v[110:111]
	v_and_b32_sdwa v104, v97, v154 dst_sel:DWORD dst_unused:UNUSED_PAD src0_sel:WORD_1 src1_sel:DWORD
	v_and_b32_sdwa v105, v96, v154 dst_sel:DWORD dst_unused:UNUSED_PAD src0_sel:WORD_1 src1_sel:DWORD
	v_and_b32_sdwa v102, v101, v154 dst_sel:DWORD dst_unused:UNUSED_PAD src0_sel:WORD_1 src1_sel:DWORD
	v_and_b32_sdwa v103, v100, v154 dst_sel:DWORD dst_unused:UNUSED_PAD src0_sel:WORD_1 src1_sel:DWORD
	v_add3_u32 v97, v97, v104, s15
	v_add3_u32 v96, v96, v105, s15
	v_add3_u32 v100, v100, v103, s15
	v_add3_u32 v101, v101, v102, s15
	v_and_b32_e32 v97, 0xffff0000, v97
	v_and_b32_e32 v96, 0xffff0000, v96
	v_or_b32_sdwa v97, v97, v101 dst_sel:DWORD dst_unused:UNUSED_PAD src0_sel:DWORD src1_sel:WORD_1
	v_or_b32_sdwa v96, v96, v100 dst_sel:DWORD dst_unused:UNUSED_PAD src0_sel:DWORD src1_sel:WORD_1
	global_store_dwordx2 v[94:95], v[96:97], off
	v_mov_b64_e32 v[100:101], v[170:171]
	v_mov_b64_e32 v[102:103], v[172:173]
	v_mov_b32_e32 v96, v90
	v_mov_b32_e32 v97, v92
	v_mov_b32_e32 v92, v91
	v_pk_mul_f32 v[90:91], v[96:97], v[108:109] op_sel_hi:[1,0]
	v_pk_mul_f32 v[92:93], v[92:93], v[108:109] op_sel_hi:[1,0]
	v_mov_b32_e32 v97, v102
	v_mov_b32_e32 v102, v101
	v_mov_b32_e32 v96, v100
	v_pk_mul_f32 v[92:93], v[92:93], v[102:103]
	v_pk_mul_f32 v[90:91], v[90:91], v[96:97]
	v_and_b32_sdwa v100, v93, v154 dst_sel:DWORD dst_unused:UNUSED_PAD src0_sel:WORD_1 src1_sel:DWORD
	v_and_b32_sdwa v101, v92, v154 dst_sel:DWORD dst_unused:UNUSED_PAD src0_sel:WORD_1 src1_sel:DWORD
	v_and_b32_sdwa v96, v91, v154 dst_sel:DWORD dst_unused:UNUSED_PAD src0_sel:WORD_1 src1_sel:DWORD
	v_and_b32_sdwa v97, v90, v154 dst_sel:DWORD dst_unused:UNUSED_PAD src0_sel:WORD_1 src1_sel:DWORD
	v_add3_u32 v93, v93, v100, s15
	v_add3_u32 v92, v92, v101, s15
	v_add3_u32 v90, v90, v97, s15
	v_add3_u32 v91, v91, v96, s15
	v_and_b32_e32 v93, 0xffff0000, v93
	v_and_b32_e32 v92, 0xffff0000, v92
	v_or_b32_sdwa v91, v93, v91 dst_sel:DWORD dst_unused:UNUSED_PAD src0_sel:DWORD src1_sel:WORD_1
	v_or_b32_sdwa v90, v92, v90 dst_sel:DWORD dst_unused:UNUSED_PAD src0_sel:DWORD src1_sel:WORD_1
	global_store_dwordx2 v[94:95], v[90:91], off offset:512
	v_mov_b64_e32 v[90:91], v[174:175]
	v_mov_b64_e32 v[92:93], v[176:177]
	v_mov_b32_e32 v96, v78
	v_mov_b32_e32 v97, v80
	v_mov_b32_e32 v80, v79
	v_pk_mul_f32 v[78:79], v[96:97], v[108:109] op_sel_hi:[1,0]
	v_pk_mul_f32 v[80:81], v[80:81], v[108:109] op_sel_hi:[1,0]
	v_mov_b32_e32 v97, v92
	v_mov_b32_e32 v92, v91
	v_mov_b32_e32 v96, v90
	v_pk_mul_f32 v[80:81], v[80:81], v[92:93]
	v_pk_mul_f32 v[78:79], v[78:79], v[96:97]
	v_and_b32_sdwa v92, v81, v154 dst_sel:DWORD dst_unused:UNUSED_PAD src0_sel:WORD_1 src1_sel:DWORD
	v_and_b32_sdwa v93, v80, v154 dst_sel:DWORD dst_unused:UNUSED_PAD src0_sel:WORD_1 src1_sel:DWORD
	v_and_b32_sdwa v90, v79, v154 dst_sel:DWORD dst_unused:UNUSED_PAD src0_sel:WORD_1 src1_sel:DWORD
	v_and_b32_sdwa v91, v78, v154 dst_sel:DWORD dst_unused:UNUSED_PAD src0_sel:WORD_1 src1_sel:DWORD
	v_add3_u32 v81, v81, v92, s15
	v_add3_u32 v80, v80, v93, s15
	v_add3_u32 v78, v78, v91, s15
	v_add3_u32 v79, v79, v90, s15
	v_and_b32_e32 v81, 0xffff0000, v81
	v_and_b32_e32 v80, 0xffff0000, v80
	v_or_b32_sdwa v79, v81, v79 dst_sel:DWORD dst_unused:UNUSED_PAD src0_sel:DWORD src1_sel:WORD_1
	v_or_b32_sdwa v78, v80, v78 dst_sel:DWORD dst_unused:UNUSED_PAD src0_sel:DWORD src1_sel:WORD_1
	global_store_dwordx2 v[94:95], v[78:79], off offset:1024
	v_mov_b64_e32 v[78:79], v[178:179]
	v_mov_b64_e32 v[80:81], v[180:181]
	v_mov_b32_e32 v90, v86
	v_mov_b32_e32 v91, v88
	v_mov_b32_e32 v88, v87
	v_pk_mul_f32 v[86:87], v[90:91], v[108:109] op_sel_hi:[1,0]
	v_pk_mul_f32 v[88:89], v[88:89], v[108:109] op_sel_hi:[1,0]
	v_mov_b32_e32 v91, v80
	v_mov_b32_e32 v80, v79
	v_mov_b32_e32 v90, v78
	v_pk_mul_f32 v[80:81], v[88:89], v[80:81]
	v_pk_mul_f32 v[78:79], v[86:87], v[90:91]
	v_and_b32_sdwa v88, v81, v154 dst_sel:DWORD dst_unused:UNUSED_PAD src0_sel:WORD_1 src1_sel:DWORD
	v_and_b32_sdwa v89, v80, v154 dst_sel:DWORD dst_unused:UNUSED_PAD src0_sel:WORD_1 src1_sel:DWORD
	v_and_b32_sdwa v86, v79, v154 dst_sel:DWORD dst_unused:UNUSED_PAD src0_sel:WORD_1 src1_sel:DWORD
	v_and_b32_sdwa v87, v78, v154 dst_sel:DWORD dst_unused:UNUSED_PAD src0_sel:WORD_1 src1_sel:DWORD
	v_add3_u32 v81, v81, v88, s15
	v_add3_u32 v80, v80, v89, s15
	v_add3_u32 v78, v78, v87, s15
	v_add3_u32 v79, v79, v86, s15
	v_and_b32_e32 v81, 0xffff0000, v81
	v_and_b32_e32 v80, 0xffff0000, v80
	v_or_b32_sdwa v79, v81, v79 dst_sel:DWORD dst_unused:UNUSED_PAD src0_sel:DWORD src1_sel:WORD_1
	v_or_b32_sdwa v78, v80, v78 dst_sel:DWORD dst_unused:UNUSED_PAD src0_sel:DWORD src1_sel:WORD_1
	global_store_dwordx2 v[94:95], v[78:79], off offset:1536
	v_mov_b64_e32 v[78:79], v[182:183]
	v_mov_b64_e32 v[80:81], v[184:185]
	v_mov_b32_e32 v86, v70
	v_mov_b32_e32 v87, v72
	v_mov_b32_e32 v72, v71
	v_pk_mul_f32 v[70:71], v[86:87], v[108:109] op_sel_hi:[1,0]
	v_pk_mul_f32 v[72:73], v[72:73], v[108:109] op_sel_hi:[1,0]
	v_mov_b32_e32 v87, v80
	v_mov_b32_e32 v80, v79
	v_mov_b32_e32 v86, v78
	v_pk_mul_f32 v[72:73], v[72:73], v[80:81]
	v_pk_mul_f32 v[70:71], v[70:71], v[86:87]
	v_and_b32_sdwa v80, v73, v154 dst_sel:DWORD dst_unused:UNUSED_PAD src0_sel:WORD_1 src1_sel:DWORD
	v_and_b32_sdwa v81, v72, v154 dst_sel:DWORD dst_unused:UNUSED_PAD src0_sel:WORD_1 src1_sel:DWORD
	v_and_b32_sdwa v78, v71, v154 dst_sel:DWORD dst_unused:UNUSED_PAD src0_sel:WORD_1 src1_sel:DWORD
	v_and_b32_sdwa v79, v70, v154 dst_sel:DWORD dst_unused:UNUSED_PAD src0_sel:WORD_1 src1_sel:DWORD
	v_add3_u32 v73, v73, v80, s15
	v_add3_u32 v72, v72, v81, s15
	v_add3_u32 v70, v70, v79, s15
	v_add3_u32 v71, v71, v78, s15
	v_and_b32_e32 v73, 0xffff0000, v73
	v_and_b32_e32 v72, 0xffff0000, v72
	v_or_b32_sdwa v71, v73, v71 dst_sel:DWORD dst_unused:UNUSED_PAD src0_sel:DWORD src1_sel:WORD_1
	v_or_b32_sdwa v70, v72, v70 dst_sel:DWORD dst_unused:UNUSED_PAD src0_sel:DWORD src1_sel:WORD_1
	global_store_dwordx2 v[94:95], v[70:71], off offset:2048
	v_mov_b64_e32 v[70:71], v[186:187]
	v_mov_b64_e32 v[72:73], v[188:189]
	v_mov_b32_e32 v79, v84
	v_mov_b32_e32 v84, v83
	v_mov_b32_e32 v78, v82
	v_pk_mul_f32 v[80:81], v[84:85], v[108:109] op_sel_hi:[1,0]
	v_pk_mul_f32 v[78:79], v[78:79], v[108:109] op_sel_hi:[1,0]
	v_mov_b32_e32 v83, v72
	v_mov_b32_e32 v72, v71
	v_mov_b32_e32 v82, v70
	v_pk_mul_f32 v[72:73], v[80:81], v[72:73]
	v_pk_mul_f32 v[70:71], v[78:79], v[82:83]
	v_and_b32_sdwa v80, v73, v154 dst_sel:DWORD dst_unused:UNUSED_PAD src0_sel:WORD_1 src1_sel:DWORD
	v_and_b32_sdwa v81, v72, v154 dst_sel:DWORD dst_unused:UNUSED_PAD src0_sel:WORD_1 src1_sel:DWORD
	v_and_b32_sdwa v78, v71, v154 dst_sel:DWORD dst_unused:UNUSED_PAD src0_sel:WORD_1 src1_sel:DWORD
	v_and_b32_sdwa v79, v70, v154 dst_sel:DWORD dst_unused:UNUSED_PAD src0_sel:WORD_1 src1_sel:DWORD
	v_add3_u32 v73, v73, v80, s15
	v_add3_u32 v72, v72, v81, s15
	v_add3_u32 v70, v70, v79, s15
	v_add3_u32 v71, v71, v78, s15
	v_and_b32_e32 v73, 0xffff0000, v73
	v_and_b32_e32 v72, 0xffff0000, v72
	v_or_b32_sdwa v71, v73, v71 dst_sel:DWORD dst_unused:UNUSED_PAD src0_sel:DWORD src1_sel:WORD_1
	v_or_b32_sdwa v70, v72, v70 dst_sel:DWORD dst_unused:UNUSED_PAD src0_sel:DWORD src1_sel:WORD_1
	global_store_dwordx2 v[94:95], v[70:71], off offset:2560
	v_mov_b64_e32 v[70:71], v[190:191]
	v_mov_b64_e32 v[72:73], v[192:193]
	v_mov_b32_e32 v78, v66
	v_mov_b32_e32 v79, v68
	v_mov_b32_e32 v68, v67
	v_pk_mul_f32 v[66:67], v[78:79], v[108:109] op_sel_hi:[1,0]
	v_pk_mul_f32 v[68:69], v[68:69], v[108:109] op_sel_hi:[1,0]
	v_mov_b32_e32 v79, v72
	v_mov_b32_e32 v72, v71
	v_mov_b32_e32 v78, v70
	v_pk_mul_f32 v[68:69], v[68:69], v[72:73]
	v_pk_mul_f32 v[66:67], v[66:67], v[78:79]
	v_and_b32_sdwa v72, v69, v154 dst_sel:DWORD dst_unused:UNUSED_PAD src0_sel:WORD_1 src1_sel:DWORD
	v_and_b32_sdwa v73, v68, v154 dst_sel:DWORD dst_unused:UNUSED_PAD src0_sel:WORD_1 src1_sel:DWORD
	v_and_b32_sdwa v70, v67, v154 dst_sel:DWORD dst_unused:UNUSED_PAD src0_sel:WORD_1 src1_sel:DWORD
	v_and_b32_sdwa v71, v66, v154 dst_sel:DWORD dst_unused:UNUSED_PAD src0_sel:WORD_1 src1_sel:DWORD
	v_add3_u32 v69, v69, v72, s15
	v_add3_u32 v68, v68, v73, s15
	v_add3_u32 v66, v66, v71, s15
	v_add3_u32 v67, v67, v70, s15
	v_and_b32_e32 v69, 0xffff0000, v69
	v_and_b32_e32 v68, 0xffff0000, v68
	v_or_b32_sdwa v67, v69, v67 dst_sel:DWORD dst_unused:UNUSED_PAD src0_sel:DWORD src1_sel:WORD_1
	v_or_b32_sdwa v66, v68, v66 dst_sel:DWORD dst_unused:UNUSED_PAD src0_sel:DWORD src1_sel:WORD_1
	global_store_dwordx2 v[94:95], v[66:67], off offset:3072
	v_mov_b64_e32 v[66:67], v[194:195]
	v_mov_b64_e32 v[68:69], v[196:197]
	v_mov_b32_e32 v71, v76
	v_mov_b32_e32 v76, v75
	v_mov_b32_e32 v70, v74
	v_pk_mul_f32 v[72:73], v[76:77], v[108:109] op_sel_hi:[1,0]
	v_pk_mul_f32 v[70:71], v[70:71], v[108:109] op_sel_hi:[1,0]
	v_mov_b32_e32 v75, v68
	v_mov_b32_e32 v68, v67
	v_mov_b32_e32 v74, v66
	v_pk_mul_f32 v[68:69], v[72:73], v[68:69]
	v_pk_mul_f32 v[66:67], v[70:71], v[74:75]
	v_and_b32_sdwa v72, v69, v154 dst_sel:DWORD dst_unused:UNUSED_PAD src0_sel:WORD_1 src1_sel:DWORD
	v_and_b32_sdwa v73, v68, v154 dst_sel:DWORD dst_unused:UNUSED_PAD src0_sel:WORD_1 src1_sel:DWORD
	v_and_b32_sdwa v70, v67, v154 dst_sel:DWORD dst_unused:UNUSED_PAD src0_sel:WORD_1 src1_sel:DWORD
	v_and_b32_sdwa v71, v66, v154 dst_sel:DWORD dst_unused:UNUSED_PAD src0_sel:WORD_1 src1_sel:DWORD
	v_add3_u32 v69, v69, v72, s15
	v_add3_u32 v68, v68, v73, s15
	v_add3_u32 v66, v66, v71, s15
	v_add3_u32 v67, v67, v70, s15
	v_and_b32_e32 v69, 0xffff0000, v69
	v_and_b32_e32 v68, 0xffff0000, v68
	v_or_b32_sdwa v67, v69, v67 dst_sel:DWORD dst_unused:UNUSED_PAD src0_sel:DWORD src1_sel:WORD_1
	v_or_b32_sdwa v66, v68, v66 dst_sel:DWORD dst_unused:UNUSED_PAD src0_sel:DWORD src1_sel:WORD_1
	global_store_dwordx2 v[94:95], v[66:67], off offset:3584
	s_and_b64 vcc, exec, s[6:7]
	s_cbranch_vccnz .LBB0_167
.LBB0_169:
	v_mov_b64_e32 v[66:67], v[166:167]
	v_mov_b64_e32 v[68:69], v[168:169]
	s_waitcnt lgkmcnt(1)
	v_add_f32_e32 v70, v106, v107
	v_fmamk_f32 v70, v70, 0x3a000000, v152
	v_mul_f32_e32 v71, 0x4f800000, v70
	v_cmp_gt_f32_e32 vcc, s11, v70
	s_lshl_b64 s[6:7], s[28:29], 12
	s_nop 0
	v_cndmask_b32_e32 v72, v70, v71, vcc
	v_sqrt_f32_e32 v73, v72
	v_mov_b32_e32 v70, v38
	v_mov_b32_e32 v71, v40
	v_mov_b32_e32 v40, v39
	v_add_u32_e32 v38, -1, v73
	v_add_u32_e32 v39, 1, v73
	v_fma_f32 v74, -v38, v73, v72
	v_fma_f32 v75, -v39, v73, v72
	v_cmp_ge_f32_e64 s[0:1], 0, v74
	s_nop 1
	v_cndmask_b32_e64 v38, v73, v38, s[0:1]
	v_cmp_lt_f32_e64 s[0:1], 0, v75
	s_nop 1
	v_cndmask_b32_e64 v38, v38, v39, s[0:1]
	v_mul_f32_e32 v39, 0x37800000, v38
	v_cndmask_b32_e32 v38, v38, v39, vcc
	v_cmp_class_f32_e32 vcc, v72, v153
	s_nop 1
	v_cndmask_b32_e32 v72, v38, v72, vcc
	v_div_scale_f32 v73, s[0:1], v72, v72, 1.0
	v_rcp_f32_e32 v74, v73
	v_div_scale_f32 v75, vcc, 1.0, v72, 1.0
	v_lshl_add_u64 v[38:39], v[148:149], 0, s[6:7]
	v_fma_f32 v76, -v73, v74, 1.0
	v_fmac_f32_e32 v74, v76, v74
	v_mul_f32_e32 v76, v75, v74
	v_fma_f32 v77, -v73, v76, v75
	v_fmac_f32_e32 v76, v77, v74
	v_fma_f32 v73, -v73, v76, v75
	v_div_fmas_f32 v73, v73, v74, v76
	v_div_fixup_f32 v72, v73, v72, 1.0
	v_pk_mul_f32 v[40:41], v[40:41], v[72:73] op_sel_hi:[1,0]
	v_pk_mul_f32 v[70:71], v[70:71], v[72:73] op_sel_hi:[1,0]
	v_mov_b32_e32 v75, v68
	v_mov_b32_e32 v68, v67
	v_mov_b32_e32 v74, v66
	v_pk_mul_f32 v[40:41], v[40:41], v[68:69]
	v_pk_mul_f32 v[66:67], v[70:71], v[74:75]
	v_and_b32_sdwa v70, v41, v154 dst_sel:DWORD dst_unused:UNUSED_PAD src0_sel:WORD_1 src1_sel:DWORD
	v_and_b32_sdwa v71, v40, v154 dst_sel:DWORD dst_unused:UNUSED_PAD src0_sel:WORD_1 src1_sel:DWORD
	v_and_b32_sdwa v68, v67, v154 dst_sel:DWORD dst_unused:UNUSED_PAD src0_sel:WORD_1 src1_sel:DWORD
	v_and_b32_sdwa v69, v66, v154 dst_sel:DWORD dst_unused:UNUSED_PAD src0_sel:WORD_1 src1_sel:DWORD
	v_add3_u32 v41, v41, v70, s15
	v_add3_u32 v40, v40, v71, s15
	v_add3_u32 v66, v66, v69, s15
	v_add3_u32 v67, v67, v68, s15
	v_and_b32_e32 v41, 0xffff0000, v41
	v_and_b32_e32 v40, 0xffff0000, v40
	v_or_b32_sdwa v41, v41, v67 dst_sel:DWORD dst_unused:UNUSED_PAD src0_sel:DWORD src1_sel:WORD_1
	v_or_b32_sdwa v40, v40, v66 dst_sel:DWORD dst_unused:UNUSED_PAD src0_sel:DWORD src1_sel:WORD_1
	global_store_dwordx2 v[38:39], v[40:41], off
	v_mov_b64_e32 v[66:67], v[170:171]
	v_mov_b64_e32 v[68:69], v[172:173]
	v_mov_b32_e32 v41, v64
	v_mov_b32_e32 v64, v63
	v_mov_b32_e32 v40, v62
	v_pk_mul_f32 v[62:63], v[64:65], v[72:73] op_sel_hi:[1,0]
	v_pk_mul_f32 v[40:41], v[40:41], v[72:73] op_sel_hi:[1,0]
	v_mov_b32_e32 v65, v68
	v_mov_b32_e32 v68, v67
	v_mov_b32_e32 v64, v66
	v_pk_mul_f32 v[62:63], v[62:63], v[68:69]
	v_pk_mul_f32 v[40:41], v[40:41], v[64:65]
	v_and_b32_sdwa v66, v63, v154 dst_sel:DWORD dst_unused:UNUSED_PAD src0_sel:WORD_1 src1_sel:DWORD
	v_and_b32_sdwa v67, v62, v154 dst_sel:DWORD dst_unused:UNUSED_PAD src0_sel:WORD_1 src1_sel:DWORD
	v_and_b32_sdwa v64, v41, v154 dst_sel:DWORD dst_unused:UNUSED_PAD src0_sel:WORD_1 src1_sel:DWORD
	v_and_b32_sdwa v65, v40, v154 dst_sel:DWORD dst_unused:UNUSED_PAD src0_sel:WORD_1 src1_sel:DWORD
	v_add3_u32 v63, v63, v66, s15
	v_add3_u32 v62, v62, v67, s15
	v_add3_u32 v40, v40, v65, s15
	v_add3_u32 v41, v41, v64, s15
	v_and_b32_e32 v63, 0xffff0000, v63
	v_and_b32_e32 v62, 0xffff0000, v62
	v_or_b32_sdwa v41, v63, v41 dst_sel:DWORD dst_unused:UNUSED_PAD src0_sel:DWORD src1_sel:WORD_1
	v_or_b32_sdwa v40, v62, v40 dst_sel:DWORD dst_unused:UNUSED_PAD src0_sel:DWORD src1_sel:WORD_1
	global_store_dwordx2 v[38:39], v[40:41], off offset:512
	v_mov_b64_e32 v[62:63], v[174:175]
	v_mov_b64_e32 v[64:65], v[176:177]
	v_mov_b32_e32 v41, v52
	v_mov_b32_e32 v52, v51
	v_mov_b32_e32 v40, v50
	v_pk_mul_f32 v[50:51], v[52:53], v[72:73] op_sel_hi:[1,0]
	v_pk_mul_f32 v[40:41], v[40:41], v[72:73] op_sel_hi:[1,0]
	v_mov_b32_e32 v53, v64
	v_mov_b32_e32 v64, v63
	v_mov_b32_e32 v52, v62
	v_pk_mul_f32 v[50:51], v[50:51], v[64:65]
	v_pk_mul_f32 v[40:41], v[40:41], v[52:53]
	v_and_b32_sdwa v62, v51, v154 dst_sel:DWORD dst_unused:UNUSED_PAD src0_sel:WORD_1 src1_sel:DWORD
	v_and_b32_sdwa v63, v50, v154 dst_sel:DWORD dst_unused:UNUSED_PAD src0_sel:WORD_1 src1_sel:DWORD
	v_and_b32_sdwa v52, v41, v154 dst_sel:DWORD dst_unused:UNUSED_PAD src0_sel:WORD_1 src1_sel:DWORD
	v_and_b32_sdwa v53, v40, v154 dst_sel:DWORD dst_unused:UNUSED_PAD src0_sel:WORD_1 src1_sel:DWORD
	v_add3_u32 v51, v51, v62, s15
	v_add3_u32 v50, v50, v63, s15
	v_add3_u32 v40, v40, v53, s15
	v_add3_u32 v41, v41, v52, s15
	v_and_b32_e32 v51, 0xffff0000, v51
	v_and_b32_e32 v50, 0xffff0000, v50
	v_or_b32_sdwa v41, v51, v41 dst_sel:DWORD dst_unused:UNUSED_PAD src0_sel:DWORD src1_sel:WORD_1
	v_or_b32_sdwa v40, v50, v40 dst_sel:DWORD dst_unused:UNUSED_PAD src0_sel:DWORD src1_sel:WORD_1
	global_store_dwordx2 v[38:39], v[40:41], off offset:1024
	v_mov_b64_e32 v[50:51], v[178:179]
	v_mov_b64_e32 v[52:53], v[180:181]
	v_mov_b32_e32 v41, v60
	v_mov_b32_e32 v60, v59
	v_mov_b32_e32 v40, v58
	v_pk_mul_f32 v[58:59], v[60:61], v[72:73] op_sel_hi:[1,0]
	v_pk_mul_f32 v[40:41], v[40:41], v[72:73] op_sel_hi:[1,0]
	v_mov_b32_e32 v61, v52
	v_mov_b32_e32 v52, v51
	v_mov_b32_e32 v60, v50
	v_pk_mul_f32 v[50:51], v[58:59], v[52:53]
	v_pk_mul_f32 v[40:41], v[40:41], v[60:61]
	v_and_b32_sdwa v58, v51, v154 dst_sel:DWORD dst_unused:UNUSED_PAD src0_sel:WORD_1 src1_sel:DWORD
	v_and_b32_sdwa v59, v50, v154 dst_sel:DWORD dst_unused:UNUSED_PAD src0_sel:WORD_1 src1_sel:DWORD
	v_and_b32_sdwa v52, v41, v154 dst_sel:DWORD dst_unused:UNUSED_PAD src0_sel:WORD_1 src1_sel:DWORD
	v_and_b32_sdwa v53, v40, v154 dst_sel:DWORD dst_unused:UNUSED_PAD src0_sel:WORD_1 src1_sel:DWORD
	v_add3_u32 v51, v51, v58, s15
	v_add3_u32 v50, v50, v59, s15
	v_add3_u32 v40, v40, v53, s15
	v_add3_u32 v41, v41, v52, s15
	v_and_b32_e32 v51, 0xffff0000, v51
	v_and_b32_e32 v50, 0xffff0000, v50
	v_or_b32_sdwa v41, v51, v41 dst_sel:DWORD dst_unused:UNUSED_PAD src0_sel:DWORD src1_sel:WORD_1
	v_or_b32_sdwa v40, v50, v40 dst_sel:DWORD dst_unused:UNUSED_PAD src0_sel:DWORD src1_sel:WORD_1
	global_store_dwordx2 v[38:39], v[40:41], off offset:1536
	v_mov_b64_e32 v[50:51], v[182:183]
	v_mov_b64_e32 v[52:53], v[184:185]
	v_mov_b32_e32 v41, v44
	v_mov_b32_e32 v44, v43
	v_mov_b32_e32 v40, v42
	v_pk_mul_f32 v[42:43], v[44:45], v[72:73] op_sel_hi:[1,0]
	v_pk_mul_f32 v[40:41], v[40:41], v[72:73] op_sel_hi:[1,0]
	v_mov_b32_e32 v45, v52
	v_mov_b32_e32 v52, v51
	v_mov_b32_e32 v44, v50
	v_pk_mul_f32 v[42:43], v[42:43], v[52:53]
	v_pk_mul_f32 v[40:41], v[40:41], v[44:45]
	v_and_b32_sdwa v50, v43, v154 dst_sel:DWORD dst_unused:UNUSED_PAD src0_sel:WORD_1 src1_sel:DWORD
	v_and_b32_sdwa v51, v42, v154 dst_sel:DWORD dst_unused:UNUSED_PAD src0_sel:WORD_1 src1_sel:DWORD
	v_and_b32_sdwa v44, v41, v154 dst_sel:DWORD dst_unused:UNUSED_PAD src0_sel:WORD_1 src1_sel:DWORD
	v_and_b32_sdwa v45, v40, v154 dst_sel:DWORD dst_unused:UNUSED_PAD src0_sel:WORD_1 src1_sel:DWORD
	v_add3_u32 v43, v43, v50, s15
	v_add3_u32 v42, v42, v51, s15
	v_add3_u32 v40, v40, v45, s15
	v_add3_u32 v41, v41, v44, s15
	v_and_b32_e32 v43, 0xffff0000, v43
	v_and_b32_e32 v42, 0xffff0000, v42
	v_or_b32_sdwa v41, v43, v41 dst_sel:DWORD dst_unused:UNUSED_PAD src0_sel:DWORD src1_sel:WORD_1
	v_or_b32_sdwa v40, v42, v40 dst_sel:DWORD dst_unused:UNUSED_PAD src0_sel:DWORD src1_sel:WORD_1
	global_store_dwordx2 v[38:39], v[40:41], off offset:2048
	v_mov_b64_e32 v[40:41], v[186:187]
	v_mov_b64_e32 v[42:43], v[188:189]
	v_mov_b32_e32 v45, v56
	v_mov_b32_e32 v56, v55
	v_mov_b32_e32 v44, v54
	v_pk_mul_f32 v[50:51], v[56:57], v[72:73] op_sel_hi:[1,0]
	v_pk_mul_f32 v[44:45], v[44:45], v[72:73] op_sel_hi:[1,0]
	v_mov_b32_e32 v53, v42
	v_mov_b32_e32 v42, v41
	v_mov_b32_e32 v52, v40
	v_pk_mul_f32 v[42:43], v[50:51], v[42:43]
	v_pk_mul_f32 v[40:41], v[44:45], v[52:53]
	v_and_b32_sdwa v50, v43, v154 dst_sel:DWORD dst_unused:UNUSED_PAD src0_sel:WORD_1 src1_sel:DWORD
	v_and_b32_sdwa v51, v42, v154 dst_sel:DWORD dst_unused:UNUSED_PAD src0_sel:WORD_1 src1_sel:DWORD
	v_and_b32_sdwa v44, v41, v154 dst_sel:DWORD dst_unused:UNUSED_PAD src0_sel:WORD_1 src1_sel:DWORD
	v_and_b32_sdwa v45, v40, v154 dst_sel:DWORD dst_unused:UNUSED_PAD src0_sel:WORD_1 src1_sel:DWORD
	v_add3_u32 v43, v43, v50, s15
	v_add3_u32 v42, v42, v51, s15
	v_add3_u32 v40, v40, v45, s15
	v_add3_u32 v41, v41, v44, s15
	v_and_b32_e32 v43, 0xffff0000, v43
	v_and_b32_e32 v42, 0xffff0000, v42
	v_or_b32_sdwa v41, v43, v41 dst_sel:DWORD dst_unused:UNUSED_PAD src0_sel:DWORD src1_sel:WORD_1
	v_or_b32_sdwa v40, v42, v40 dst_sel:DWORD dst_unused:UNUSED_PAD src0_sel:DWORD src1_sel:WORD_1
	global_store_dwordx2 v[38:39], v[40:41], off offset:2560
	v_mov_b64_e32 v[40:41], v[190:191]
	v_mov_b64_e32 v[42:43], v[192:193]
	v_mov_b32_e32 v44, v34
	v_mov_b32_e32 v45, v36
	v_mov_b32_e32 v36, v35
	v_pk_mul_f32 v[34:35], v[44:45], v[72:73] op_sel_hi:[1,0]
	v_pk_mul_f32 v[36:37], v[36:37], v[72:73] op_sel_hi:[1,0]
	v_mov_b32_e32 v45, v42
	v_mov_b32_e32 v42, v41
	v_mov_b32_e32 v44, v40
	v_pk_mul_f32 v[36:37], v[36:37], v[42:43]
	v_pk_mul_f32 v[34:35], v[34:35], v[44:45]
	v_and_b32_sdwa v42, v37, v154 dst_sel:DWORD dst_unused:UNUSED_PAD src0_sel:WORD_1 src1_sel:DWORD
	v_and_b32_sdwa v43, v36, v154 dst_sel:DWORD dst_unused:UNUSED_PAD src0_sel:WORD_1 src1_sel:DWORD
	v_and_b32_sdwa v40, v35, v154 dst_sel:DWORD dst_unused:UNUSED_PAD src0_sel:WORD_1 src1_sel:DWORD
	v_and_b32_sdwa v41, v34, v154 dst_sel:DWORD dst_unused:UNUSED_PAD src0_sel:WORD_1 src1_sel:DWORD
	v_add3_u32 v37, v37, v42, s15
	v_add3_u32 v36, v36, v43, s15
	v_add3_u32 v34, v34, v41, s15
	v_add3_u32 v35, v35, v40, s15
	v_and_b32_e32 v37, 0xffff0000, v37
	v_and_b32_e32 v36, 0xffff0000, v36
	v_or_b32_sdwa v35, v37, v35 dst_sel:DWORD dst_unused:UNUSED_PAD src0_sel:DWORD src1_sel:WORD_1
	v_or_b32_sdwa v34, v36, v34 dst_sel:DWORD dst_unused:UNUSED_PAD src0_sel:DWORD src1_sel:WORD_1
	global_store_dwordx2 v[38:39], v[34:35], off offset:3072
	v_mov_b64_e32 v[34:35], v[194:195]
	v_mov_b64_e32 v[36:37], v[196:197]
	v_mov_b32_e32 v41, v48
	v_mov_b32_e32 v48, v47
	v_mov_b32_e32 v40, v46
	v_pk_mul_f32 v[42:43], v[48:49], v[72:73] op_sel_hi:[1,0]
	v_pk_mul_f32 v[40:41], v[40:41], v[72:73] op_sel_hi:[1,0]
	v_mov_b32_e32 v45, v36
	v_mov_b32_e32 v36, v35
	v_mov_b32_e32 v44, v34
	v_pk_mul_f32 v[36:37], v[42:43], v[36:37]
	v_pk_mul_f32 v[34:35], v[40:41], v[44:45]
	v_and_b32_sdwa v42, v37, v154 dst_sel:DWORD dst_unused:UNUSED_PAD src0_sel:WORD_1 src1_sel:DWORD
	v_and_b32_sdwa v43, v36, v154 dst_sel:DWORD dst_unused:UNUSED_PAD src0_sel:WORD_1 src1_sel:DWORD
	v_and_b32_sdwa v40, v35, v154 dst_sel:DWORD dst_unused:UNUSED_PAD src0_sel:WORD_1 src1_sel:DWORD
	v_and_b32_sdwa v41, v34, v154 dst_sel:DWORD dst_unused:UNUSED_PAD src0_sel:WORD_1 src1_sel:DWORD
	v_add3_u32 v37, v37, v42, s15
	v_add3_u32 v36, v36, v43, s15
	v_add3_u32 v34, v34, v41, s15
	v_add3_u32 v35, v35, v40, s15
	v_and_b32_e32 v37, 0xffff0000, v37
	v_and_b32_e32 v36, 0xffff0000, v36
	v_or_b32_sdwa v35, v37, v35 dst_sel:DWORD dst_unused:UNUSED_PAD src0_sel:DWORD src1_sel:WORD_1
	v_or_b32_sdwa v34, v36, v34 dst_sel:DWORD dst_unused:UNUSED_PAD src0_sel:DWORD src1_sel:WORD_1
	global_store_dwordx2 v[38:39], v[34:35], off offset:3584
	s_and_b64 vcc, exec, s[4:5]
	s_cbranch_vccnz .LBB0_116
.LBB0_170:
	v_mov_b64_e32 v[34:35], v[166:167]
	v_mov_b64_e32 v[36:37], v[168:169]
	s_waitcnt lgkmcnt(0)
	v_add_f32_e32 v38, v98, v99
	v_fmamk_f32 v38, v38, 0x3a000000, v152
	v_mul_f32_e32 v39, 0x4f800000, v38
	v_cmp_gt_f32_e32 vcc, s11, v38
	s_lshl_b64 s[4:5], s[26:27], 12
	s_nop 0
	v_cndmask_b32_e32 v40, v38, v39, vcc
	v_sqrt_f32_e32 v41, v40
	v_mov_b32_e32 v38, v6
	v_mov_b32_e32 v39, v8
	v_mov_b32_e32 v8, v7
	v_add_u32_e32 v6, -1, v41
	v_add_u32_e32 v7, 1, v41
	v_fma_f32 v42, -v6, v41, v40
	v_fma_f32 v43, -v7, v41, v40
	v_cmp_ge_f32_e64 s[0:1], 0, v42
	s_nop 1
	v_cndmask_b32_e64 v6, v41, v6, s[0:1]
	v_cmp_lt_f32_e64 s[0:1], 0, v43
	s_nop 1
	v_cndmask_b32_e64 v6, v6, v7, s[0:1]
	v_mul_f32_e32 v7, 0x37800000, v6
	v_cndmask_b32_e32 v6, v6, v7, vcc
	v_cmp_class_f32_e32 vcc, v40, v153
	s_nop 1
	v_cndmask_b32_e32 v40, v6, v40, vcc
	v_div_scale_f32 v41, s[0:1], v40, v40, 1.0
	v_rcp_f32_e32 v42, v41
	v_div_scale_f32 v43, vcc, 1.0, v40, 1.0
	v_lshl_add_u64 v[6:7], v[148:149], 0, s[4:5]
	v_fma_f32 v44, -v41, v42, 1.0
	v_fmac_f32_e32 v42, v44, v42
	v_mul_f32_e32 v44, v43, v42
	v_fma_f32 v45, -v41, v44, v43
	v_fmac_f32_e32 v44, v45, v42
	v_fma_f32 v41, -v41, v44, v43
	v_div_fmas_f32 v41, v41, v42, v44
	v_div_fixup_f32 v40, v41, v40, 1.0
	v_pk_mul_f32 v[8:9], v[8:9], v[40:41] op_sel_hi:[1,0]
	v_pk_mul_f32 v[38:39], v[38:39], v[40:41] op_sel_hi:[1,0]
	v_mov_b32_e32 v43, v36
	v_mov_b32_e32 v36, v35
	v_mov_b32_e32 v42, v34
	v_pk_mul_f32 v[8:9], v[8:9], v[36:37]
	v_pk_mul_f32 v[34:35], v[38:39], v[42:43]
	v_and_b32_sdwa v38, v9, v154 dst_sel:DWORD dst_unused:UNUSED_PAD src0_sel:WORD_1 src1_sel:DWORD
	v_and_b32_sdwa v39, v8, v154 dst_sel:DWORD dst_unused:UNUSED_PAD src0_sel:WORD_1 src1_sel:DWORD
	v_and_b32_sdwa v36, v35, v154 dst_sel:DWORD dst_unused:UNUSED_PAD src0_sel:WORD_1 src1_sel:DWORD
	v_and_b32_sdwa v37, v34, v154 dst_sel:DWORD dst_unused:UNUSED_PAD src0_sel:WORD_1 src1_sel:DWORD
	v_add3_u32 v9, v9, v38, s15
	v_add3_u32 v8, v8, v39, s15
	v_add3_u32 v34, v34, v37, s15
	v_add3_u32 v35, v35, v36, s15
	v_and_b32_e32 v9, 0xffff0000, v9
	v_and_b32_e32 v8, 0xffff0000, v8
	v_or_b32_sdwa v9, v9, v35 dst_sel:DWORD dst_unused:UNUSED_PAD src0_sel:DWORD src1_sel:WORD_1
	v_or_b32_sdwa v8, v8, v34 dst_sel:DWORD dst_unused:UNUSED_PAD src0_sel:DWORD src1_sel:WORD_1
	global_store_dwordx2 v[6:7], v[8:9], off
	v_mov_b64_e32 v[34:35], v[170:171]
	v_mov_b64_e32 v[36:37], v[172:173]
	v_mov_b32_e32 v9, v32
	v_mov_b32_e32 v32, v31
	v_mov_b32_e32 v8, v30
	v_pk_mul_f32 v[30:31], v[32:33], v[40:41] op_sel_hi:[1,0]
	v_pk_mul_f32 v[8:9], v[8:9], v[40:41] op_sel_hi:[1,0]
	v_mov_b32_e32 v33, v36
	v_mov_b32_e32 v36, v35
	v_mov_b32_e32 v32, v34
	v_pk_mul_f32 v[30:31], v[30:31], v[36:37]
	v_pk_mul_f32 v[8:9], v[8:9], v[32:33]
	v_and_b32_sdwa v34, v31, v154 dst_sel:DWORD dst_unused:UNUSED_PAD src0_sel:WORD_1 src1_sel:DWORD
	v_and_b32_sdwa v35, v30, v154 dst_sel:DWORD dst_unused:UNUSED_PAD src0_sel:WORD_1 src1_sel:DWORD
	v_and_b32_sdwa v32, v9, v154 dst_sel:DWORD dst_unused:UNUSED_PAD src0_sel:WORD_1 src1_sel:DWORD
	v_and_b32_sdwa v33, v8, v154 dst_sel:DWORD dst_unused:UNUSED_PAD src0_sel:WORD_1 src1_sel:DWORD
	v_add3_u32 v31, v31, v34, s15
	v_add3_u32 v30, v30, v35, s15
	v_add3_u32 v8, v8, v33, s15
	v_add3_u32 v9, v9, v32, s15
	v_and_b32_e32 v31, 0xffff0000, v31
	v_and_b32_e32 v30, 0xffff0000, v30
	v_or_b32_sdwa v9, v31, v9 dst_sel:DWORD dst_unused:UNUSED_PAD src0_sel:DWORD src1_sel:WORD_1
	v_or_b32_sdwa v8, v30, v8 dst_sel:DWORD dst_unused:UNUSED_PAD src0_sel:DWORD src1_sel:WORD_1
	global_store_dwordx2 v[6:7], v[8:9], off offset:512
	v_mov_b64_e32 v[30:31], v[174:175]
	v_mov_b64_e32 v[32:33], v[176:177]
	v_mov_b32_e32 v9, v20
	v_mov_b32_e32 v20, v19
	v_mov_b32_e32 v8, v18
	v_pk_mul_f32 v[18:19], v[20:21], v[40:41] op_sel_hi:[1,0]
	v_pk_mul_f32 v[8:9], v[8:9], v[40:41] op_sel_hi:[1,0]
	v_mov_b32_e32 v21, v32
	v_mov_b32_e32 v32, v31
	v_mov_b32_e32 v20, v30
	v_pk_mul_f32 v[18:19], v[18:19], v[32:33]
	v_pk_mul_f32 v[8:9], v[8:9], v[20:21]
	v_and_b32_sdwa v30, v19, v154 dst_sel:DWORD dst_unused:UNUSED_PAD src0_sel:WORD_1 src1_sel:DWORD
	v_and_b32_sdwa v31, v18, v154 dst_sel:DWORD dst_unused:UNUSED_PAD src0_sel:WORD_1 src1_sel:DWORD
	v_and_b32_sdwa v20, v9, v154 dst_sel:DWORD dst_unused:UNUSED_PAD src0_sel:WORD_1 src1_sel:DWORD
	v_and_b32_sdwa v21, v8, v154 dst_sel:DWORD dst_unused:UNUSED_PAD src0_sel:WORD_1 src1_sel:DWORD
	v_add3_u32 v19, v19, v30, s15
	v_add3_u32 v18, v18, v31, s15
	v_add3_u32 v8, v8, v21, s15
	v_add3_u32 v9, v9, v20, s15
	v_and_b32_e32 v19, 0xffff0000, v19
	v_and_b32_e32 v18, 0xffff0000, v18
	v_or_b32_sdwa v9, v19, v9 dst_sel:DWORD dst_unused:UNUSED_PAD src0_sel:DWORD src1_sel:WORD_1
	v_or_b32_sdwa v8, v18, v8 dst_sel:DWORD dst_unused:UNUSED_PAD src0_sel:DWORD src1_sel:WORD_1
	global_store_dwordx2 v[6:7], v[8:9], off offset:1024
	v_mov_b64_e32 v[18:19], v[178:179]
	v_mov_b64_e32 v[20:21], v[180:181]
	v_mov_b32_e32 v9, v28
	v_mov_b32_e32 v28, v27
	v_mov_b32_e32 v8, v26
	v_pk_mul_f32 v[26:27], v[28:29], v[40:41] op_sel_hi:[1,0]
	v_pk_mul_f32 v[8:9], v[8:9], v[40:41] op_sel_hi:[1,0]
	v_mov_b32_e32 v29, v20
	v_mov_b32_e32 v20, v19
	v_mov_b32_e32 v28, v18
	v_pk_mul_f32 v[18:19], v[26:27], v[20:21]
	v_pk_mul_f32 v[8:9], v[8:9], v[28:29]
	v_and_b32_sdwa v26, v19, v154 dst_sel:DWORD dst_unused:UNUSED_PAD src0_sel:WORD_1 src1_sel:DWORD
	v_and_b32_sdwa v27, v18, v154 dst_sel:DWORD dst_unused:UNUSED_PAD src0_sel:WORD_1 src1_sel:DWORD
	v_and_b32_sdwa v20, v9, v154 dst_sel:DWORD dst_unused:UNUSED_PAD src0_sel:WORD_1 src1_sel:DWORD
	v_and_b32_sdwa v21, v8, v154 dst_sel:DWORD dst_unused:UNUSED_PAD src0_sel:WORD_1 src1_sel:DWORD
	v_add3_u32 v19, v19, v26, s15
	v_add3_u32 v18, v18, v27, s15
	v_add3_u32 v8, v8, v21, s15
	v_add3_u32 v9, v9, v20, s15
	v_and_b32_e32 v19, 0xffff0000, v19
	v_and_b32_e32 v18, 0xffff0000, v18
	v_or_b32_sdwa v9, v19, v9 dst_sel:DWORD dst_unused:UNUSED_PAD src0_sel:DWORD src1_sel:WORD_1
	v_or_b32_sdwa v8, v18, v8 dst_sel:DWORD dst_unused:UNUSED_PAD src0_sel:DWORD src1_sel:WORD_1
	global_store_dwordx2 v[6:7], v[8:9], off offset:1536
	v_mov_b64_e32 v[18:19], v[182:183]
	v_mov_b64_e32 v[20:21], v[184:185]
	v_mov_b32_e32 v9, v12
	v_mov_b32_e32 v12, v11
	v_mov_b32_e32 v8, v10
	v_pk_mul_f32 v[10:11], v[12:13], v[40:41] op_sel_hi:[1,0]
	v_pk_mul_f32 v[8:9], v[8:9], v[40:41] op_sel_hi:[1,0]
	v_mov_b32_e32 v13, v20
	v_mov_b32_e32 v20, v19
	v_mov_b32_e32 v12, v18
	v_pk_mul_f32 v[10:11], v[10:11], v[20:21]
	v_pk_mul_f32 v[8:9], v[8:9], v[12:13]
	v_and_b32_sdwa v18, v11, v154 dst_sel:DWORD dst_unused:UNUSED_PAD src0_sel:WORD_1 src1_sel:DWORD
	v_and_b32_sdwa v19, v10, v154 dst_sel:DWORD dst_unused:UNUSED_PAD src0_sel:WORD_1 src1_sel:DWORD
	v_and_b32_sdwa v12, v9, v154 dst_sel:DWORD dst_unused:UNUSED_PAD src0_sel:WORD_1 src1_sel:DWORD
	v_and_b32_sdwa v13, v8, v154 dst_sel:DWORD dst_unused:UNUSED_PAD src0_sel:WORD_1 src1_sel:DWORD
	v_add3_u32 v11, v11, v18, s15
	v_add3_u32 v10, v10, v19, s15
	v_add3_u32 v8, v8, v13, s15
	v_add3_u32 v9, v9, v12, s15
	v_and_b32_e32 v11, 0xffff0000, v11
	v_and_b32_e32 v10, 0xffff0000, v10
	v_or_b32_sdwa v9, v11, v9 dst_sel:DWORD dst_unused:UNUSED_PAD src0_sel:DWORD src1_sel:WORD_1
	v_or_b32_sdwa v8, v10, v8 dst_sel:DWORD dst_unused:UNUSED_PAD src0_sel:DWORD src1_sel:WORD_1
	global_store_dwordx2 v[6:7], v[8:9], off offset:2048
	v_mov_b64_e32 v[8:9], v[186:187]
	v_mov_b64_e32 v[10:11], v[188:189]
	v_mov_b32_e32 v13, v24
	v_mov_b32_e32 v24, v23
	v_mov_b32_e32 v12, v22
	v_pk_mul_f32 v[18:19], v[24:25], v[40:41] op_sel_hi:[1,0]
	v_pk_mul_f32 v[12:13], v[12:13], v[40:41] op_sel_hi:[1,0]
	v_mov_b32_e32 v21, v10
	v_mov_b32_e32 v10, v9
	v_mov_b32_e32 v20, v8
	v_pk_mul_f32 v[10:11], v[18:19], v[10:11]
	v_pk_mul_f32 v[8:9], v[12:13], v[20:21]
	v_and_b32_sdwa v18, v11, v154 dst_sel:DWORD dst_unused:UNUSED_PAD src0_sel:WORD_1 src1_sel:DWORD
	v_and_b32_sdwa v19, v10, v154 dst_sel:DWORD dst_unused:UNUSED_PAD src0_sel:WORD_1 src1_sel:DWORD
	v_and_b32_sdwa v12, v9, v154 dst_sel:DWORD dst_unused:UNUSED_PAD src0_sel:WORD_1 src1_sel:DWORD
	v_and_b32_sdwa v13, v8, v154 dst_sel:DWORD dst_unused:UNUSED_PAD src0_sel:WORD_1 src1_sel:DWORD
	v_add3_u32 v11, v11, v18, s15
	v_add3_u32 v10, v10, v19, s15
	v_add3_u32 v8, v8, v13, s15
	v_add3_u32 v9, v9, v12, s15
	v_and_b32_e32 v11, 0xffff0000, v11
	v_and_b32_e32 v10, 0xffff0000, v10
	v_or_b32_sdwa v9, v11, v9 dst_sel:DWORD dst_unused:UNUSED_PAD src0_sel:DWORD src1_sel:WORD_1
	v_or_b32_sdwa v8, v10, v8 dst_sel:DWORD dst_unused:UNUSED_PAD src0_sel:DWORD src1_sel:WORD_1
	global_store_dwordx2 v[6:7], v[8:9], off offset:2560
	v_mov_b64_e32 v[8:9], v[190:191]
	v_mov_b64_e32 v[10:11], v[192:193]
	v_mov_b32_e32 v12, v2
	v_mov_b32_e32 v13, v4
	v_mov_b32_e32 v4, v3
	v_pk_mul_f32 v[2:3], v[12:13], v[40:41] op_sel_hi:[1,0]
	v_pk_mul_f32 v[4:5], v[4:5], v[40:41] op_sel_hi:[1,0]
	v_mov_b32_e32 v13, v10
	v_mov_b32_e32 v10, v9
	v_mov_b32_e32 v12, v8
	v_pk_mul_f32 v[4:5], v[4:5], v[10:11]
	v_pk_mul_f32 v[2:3], v[2:3], v[12:13]
	v_and_b32_sdwa v10, v5, v154 dst_sel:DWORD dst_unused:UNUSED_PAD src0_sel:WORD_1 src1_sel:DWORD
	v_and_b32_sdwa v11, v4, v154 dst_sel:DWORD dst_unused:UNUSED_PAD src0_sel:WORD_1 src1_sel:DWORD
	v_and_b32_sdwa v8, v3, v154 dst_sel:DWORD dst_unused:UNUSED_PAD src0_sel:WORD_1 src1_sel:DWORD
	v_and_b32_sdwa v9, v2, v154 dst_sel:DWORD dst_unused:UNUSED_PAD src0_sel:WORD_1 src1_sel:DWORD
	v_add3_u32 v5, v5, v10, s15
	v_add3_u32 v4, v4, v11, s15
	v_add3_u32 v2, v2, v9, s15
	v_add3_u32 v3, v3, v8, s15
	v_and_b32_e32 v5, 0xffff0000, v5
	v_and_b32_e32 v4, 0xffff0000, v4
	v_or_b32_sdwa v3, v5, v3 dst_sel:DWORD dst_unused:UNUSED_PAD src0_sel:DWORD src1_sel:WORD_1
	v_or_b32_sdwa v2, v4, v2 dst_sel:DWORD dst_unused:UNUSED_PAD src0_sel:DWORD src1_sel:WORD_1
	global_store_dwordx2 v[6:7], v[2:3], off offset:3072
	v_mov_b64_e32 v[2:3], v[194:195]
	v_mov_b64_e32 v[4:5], v[196:197]
	v_mov_b32_e32 v9, v16
	v_mov_b32_e32 v16, v15
	v_mov_b32_e32 v8, v14
	v_pk_mul_f32 v[10:11], v[16:17], v[40:41] op_sel_hi:[1,0]
	v_pk_mul_f32 v[8:9], v[8:9], v[40:41] op_sel_hi:[1,0]
	v_mov_b32_e32 v13, v4
	v_mov_b32_e32 v4, v3
	v_mov_b32_e32 v12, v2
	v_pk_mul_f32 v[4:5], v[10:11], v[4:5]
	v_pk_mul_f32 v[2:3], v[8:9], v[12:13]
	v_and_b32_sdwa v10, v5, v154 dst_sel:DWORD dst_unused:UNUSED_PAD src0_sel:WORD_1 src1_sel:DWORD
	v_and_b32_sdwa v11, v4, v154 dst_sel:DWORD dst_unused:UNUSED_PAD src0_sel:WORD_1 src1_sel:DWORD
	v_and_b32_sdwa v8, v3, v154 dst_sel:DWORD dst_unused:UNUSED_PAD src0_sel:WORD_1 src1_sel:DWORD
	v_and_b32_sdwa v9, v2, v154 dst_sel:DWORD dst_unused:UNUSED_PAD src0_sel:WORD_1 src1_sel:DWORD
	v_add3_u32 v5, v5, v10, s15
	v_add3_u32 v4, v4, v11, s15
	v_add3_u32 v2, v2, v9, s15
	v_add3_u32 v3, v3, v8, s15
	v_and_b32_e32 v5, 0xffff0000, v5
	v_and_b32_e32 v4, 0xffff0000, v4
	v_or_b32_sdwa v3, v5, v3 dst_sel:DWORD dst_unused:UNUSED_PAD src0_sel:DWORD src1_sel:WORD_1
	v_or_b32_sdwa v2, v4, v2 dst_sel:DWORD dst_unused:UNUSED_PAD src0_sel:DWORD src1_sel:WORD_1
	global_store_dwordx2 v[6:7], v[2:3], off offset:3584
	s_branch .LBB0_116

.LBB0_1846:
	s_or_b64 exec, exec, s[20:21]
	s_andn2_b64 vcc, exec, s[18:19]
	s_mov_b32 s20, s24
	s_mov_b32 s21, s11
	s_waitcnt lgkmcnt(0)
	s_barrier
	s_cbranch_vccnz .LBB0_1800
	global_load_dwordx4 v[166:169], v[6:7], off
	global_load_dwordx4 v[170:173], v[6:7], off offset:1024
	global_load_dwordx4 v[174:177], v[6:7], off offset:2048
	global_load_dwordx4 v[178:181], v[6:7], off offset:3072
	global_load_dwordx4 v[182:185], v[8:9], off
	global_load_dwordx4 v[186:189], v[10:11], off
	global_load_dwordx4 v[190:193], v[12:13], off
	global_load_dwordx4 v[194:197], v[14:15], off
	s_waitcnt vmcnt(0)
.LBB0_1847:
	v_mov_b32_e32 v5, s20
	ds_read_b96 v[40:42], v5
	s_waitcnt lgkmcnt(0)
	v_readfirstlane_b32 s2, v40
	s_ashr_i32 s3, s2, 31
	s_lshl_b64 s[22:23], s[2:3], 2
	s_add_u32 s22, s9, s22
	s_addc_u32 s23, s10, s23
	s_lshl_b64 s[2:3], s[2:3], 12
	v_lshl_add_u64 v[22:23], v[16:17], 0, s[2:3]
	v_ashrrev_i32_e32 v35, 31, v41
	v_mov_b32_e32 v34, v41
	v_ashrrev_i32_e32 v41, 31, v42
	v_mov_b32_e32 v40, v42
	global_load_dword v20, v4, s[22:23]
	global_load_dwordx2 v[30:31], v[22:23], off
	global_load_dwordx2 v[44:45], v[22:23], off offset:512
	global_load_dwordx2 v[36:37], v[22:23], off offset:1024
	global_load_dwordx2 v[32:33], v[22:23], off offset:1536
	global_load_dwordx2 v[28:29], v[22:23], off offset:2048
	global_load_dwordx2 v[26:27], v[22:23], off offset:2560
	global_load_dwordx2 v[24:25], v[22:23], off offset:3072
	s_nop 0
	global_load_dwordx2 v[22:23], v[22:23], off offset:3584
	v_lshlrev_b64 v[46:47], 12, v[40:41]
	v_mov_b64_e32 v[40:41], v[166:167]
	v_mov_b64_e32 v[42:43], v[168:169]
	v_lshlrev_b64 v[34:35], 12, v[34:35]
	s_add_i32 s21, s21, 8
	s_addk_i32 s20, 0x80
	s_cmp_gt_i32 s21, 55
	s_waitcnt vmcnt(7)
	v_lshlrev_b32_e32 v48, 16, v30
	v_and_b32_e32 v49, 0xffff0000, v30
	v_lshlrev_b32_e32 v30, 16, v31
	v_and_b32_e32 v31, 0xffff0000, v31
	s_waitcnt vmcnt(0)
	v_pk_mul_f32 v[40:41], v[40:41], v[48:49]
	v_pk_mul_f32 v[30:31], v[42:43], v[30:31]
	v_pk_mul_f32 v[40:41], v[20:21], v[40:41] op_sel_hi:[0,1]
	v_pk_mul_f32 v[30:31], v[20:21], v[30:31] op_sel_hi:[0,1]
	v_cvt_pk_bf16_f32 v40, v40, v41
	v_cvt_pk_bf16_f32 v41, v30, v31
	v_lshl_add_u64 v[30:31], v[18:19], 0, v[34:35]
	v_lshl_add_u64 v[34:35], v[18:19], 0, v[46:47]
	global_store_dwordx2 v[30:31], v[40:41], off
	global_store_dwordx2 v[34:35], v[40:41], off
	v_mov_b64_e32 v[40:41], v[170:171]
	v_mov_b64_e32 v[42:43], v[172:173]
	v_lshlrev_b32_e32 v46, 16, v44
	v_and_b32_e32 v47, 0xffff0000, v44
	v_lshlrev_b32_e32 v44, 16, v45
	v_and_b32_e32 v45, 0xffff0000, v45
	v_pk_mul_f32 v[40:41], v[40:41], v[46:47]
	v_pk_mul_f32 v[42:43], v[42:43], v[44:45]
	v_pk_mul_f32 v[40:41], v[20:21], v[40:41] op_sel_hi:[0,1]
	v_pk_mul_f32 v[42:43], v[20:21], v[42:43] op_sel_hi:[0,1]
	v_cvt_pk_bf16_f32 v40, v40, v41
	v_cvt_pk_bf16_f32 v41, v42, v43
	global_store_dwordx2 v[30:31], v[40:41], off offset:512
	global_store_dwordx2 v[34:35], v[40:41], off offset:512
	v_mov_b64_e32 v[40:41], v[174:175]
	v_mov_b64_e32 v[42:43], v[176:177]
	v_lshlrev_b32_e32 v44, 16, v36
	v_and_b32_e32 v45, 0xffff0000, v36
	v_pk_mul_f32 v[40:41], v[40:41], v[44:45]
	s_nop 0
	v_pk_mul_f32 v[40:41], v[20:21], v[40:41] op_sel_hi:[0,1]
	v_cvt_pk_bf16_f32 v36, v40, v41
	v_lshlrev_b32_e32 v40, 16, v37
	v_and_b32_e32 v41, 0xffff0000, v37
	v_pk_mul_f32 v[40:41], v[42:43], v[40:41]
	s_nop 0
	v_pk_mul_f32 v[40:41], v[20:21], v[40:41] op_sel_hi:[0,1]
	v_cvt_pk_bf16_f32 v37, v40, v41
	global_store_dwordx2 v[30:31], v[36:37], off offset:1024
	global_store_dwordx2 v[34:35], v[36:37], off offset:1024
	v_mov_b64_e32 v[40:41], v[178:179]
	v_mov_b64_e32 v[42:43], v[180:181]
	v_lshlrev_b32_e32 v36, 16, v32
	v_and_b32_e32 v37, 0xffff0000, v32
	v_pk_mul_f32 v[36:37], v[40:41], v[36:37]
	s_nop 0
	v_pk_mul_f32 v[36:37], v[20:21], v[36:37] op_sel_hi:[0,1]
	v_cvt_pk_bf16_f32 v32, v36, v37
	v_lshlrev_b32_e32 v36, 16, v33
	v_and_b32_e32 v37, 0xffff0000, v33
	v_pk_mul_f32 v[36:37], v[42:43], v[36:37]
	s_nop 0
	v_pk_mul_f32 v[36:37], v[20:21], v[36:37] op_sel_hi:[0,1]
	v_cvt_pk_bf16_f32 v33, v36, v37
	global_store_dwordx2 v[30:31], v[32:33], off offset:1536
	global_store_dwordx2 v[34:35], v[32:33], off offset:1536
	v_mov_b64_e32 v[40:41], v[182:183]
	v_mov_b64_e32 v[42:43], v[184:185]
	v_lshlrev_b32_e32 v32, 16, v28
	v_and_b32_e32 v33, 0xffff0000, v28
	v_pk_mul_f32 v[32:33], v[40:41], v[32:33]
	s_nop 0
	v_pk_mul_f32 v[32:33], v[20:21], v[32:33] op_sel_hi:[0,1]
	v_cvt_pk_bf16_f32 v28, v32, v33
	v_lshlrev_b32_e32 v32, 16, v29
	v_and_b32_e32 v33, 0xffff0000, v29
	v_pk_mul_f32 v[32:33], v[42:43], v[32:33]
	s_nop 0
	v_pk_mul_f32 v[32:33], v[20:21], v[32:33] op_sel_hi:[0,1]
	v_cvt_pk_bf16_f32 v29, v32, v33
	global_store_dwordx2 v[30:31], v[28:29], off offset:2048
	global_store_dwordx2 v[34:35], v[28:29], off offset:2048
	v_mov_b64_e32 v[40:41], v[186:187]
	v_mov_b64_e32 v[42:43], v[188:189]
	v_lshlrev_b32_e32 v28, 16, v26
	v_and_b32_e32 v29, 0xffff0000, v26
	v_lshlrev_b32_e32 v32, 16, v24
	v_and_b32_e32 v33, 0xffff0000, v24
	v_pk_mul_f32 v[28:29], v[40:41], v[28:29]
	s_nop 0
	v_pk_mul_f32 v[28:29], v[20:21], v[28:29] op_sel_hi:[0,1]
	v_cvt_pk_bf16_f32 v26, v28, v29
	v_lshlrev_b32_e32 v28, 16, v27
	v_and_b32_e32 v29, 0xffff0000, v27
	v_pk_mul_f32 v[28:29], v[42:43], v[28:29]
	s_nop 0
	v_pk_mul_f32 v[28:29], v[20:21], v[28:29] op_sel_hi:[0,1]
	v_cvt_pk_bf16_f32 v27, v28, v29
	global_store_dwordx2 v[30:31], v[26:27], off offset:2560
	global_store_dwordx2 v[34:35], v[26:27], off offset:2560
	v_mov_b64_e32 v[26:27], v[190:191]
	v_mov_b64_e32 v[28:29], v[192:193]
	v_pk_mul_f32 v[26:27], v[26:27], v[32:33]
	s_nop 0
	v_pk_mul_f32 v[26:27], v[20:21], v[26:27] op_sel_hi:[0,1]
	v_cvt_pk_bf16_f32 v24, v26, v27
	v_lshlrev_b32_e32 v26, 16, v25
	v_and_b32_e32 v27, 0xffff0000, v25
	v_pk_mul_f32 v[26:27], v[28:29], v[26:27]
	v_lshlrev_b32_e32 v28, 16, v22
	v_pk_mul_f32 v[26:27], v[20:21], v[26:27] op_sel_hi:[0,1]
	v_cvt_pk_bf16_f32 v25, v26, v27
	global_store_dwordx2 v[30:31], v[24:25], off offset:3072
	global_store_dwordx2 v[34:35], v[24:25], off offset:3072
	v_mov_b64_e32 v[24:25], v[194:195]
	v_mov_b64_e32 v[26:27], v[196:197]
	v_and_b32_e32 v29, 0xffff0000, v22
	v_pk_mul_f32 v[24:25], v[24:25], v[28:29]
	s_nop 0
	v_pk_mul_f32 v[24:25], v[20:21], v[24:25] op_sel_hi:[0,1]
	v_cvt_pk_bf16_f32 v22, v24, v25
	v_lshlrev_b32_e32 v24, 16, v23
	v_and_b32_e32 v25, 0xffff0000, v23
	v_pk_mul_f32 v[24:25], v[26:27], v[24:25]
	s_nop 0
	v_pk_mul_f32 v[20:21], v[20:21], v[24:25] op_sel_hi:[0,1]
	v_cvt_pk_bf16_f32 v23, v20, v21
	global_store_dwordx2 v[30:31], v[22:23], off offset:3584
	global_store_dwordx2 v[34:35], v[22:23], off offset:3584
	s_cbranch_scc0 .LBB0_1847
	s_branch .LBB0_1800

.LBB0_2408:
	v_readlane_b32 s44, v233, 0
	v_readlane_b32 s48, v233, 4
	v_readlane_b32 s49, v233, 5
	s_lshl_b64 s[0:1], s[0:1], 2
	v_readlane_b32 s50, v233, 6
	v_readlane_b32 s51, v233, 7
	v_readlane_b32 s52, v233, 8
	v_readlane_b32 s53, v233, 9
	v_readlane_b32 s54, v233, 10
	v_readlane_b32 s55, v233, 11
	v_readlane_b32 s56, v233, 12
	v_readlane_b32 s57, v233, 13
	v_readlane_b32 s58, v233, 14
	v_readlane_b32 s59, v233, 15
	s_mov_b64 s[20:21], s[48:49]
	s_add_u32 s16, s20, s0
	s_addc_u32 s17, s21, s1
	s_cmpk_lt_i32 s4, 0x4000
	s_cselect_b64 s[2:3], -1, 0
	v_cndmask_b32_e64 v1, 0, 1, s[2:3]
	s_mov_b64 s[0:1], -1
	s_andn2_b64 vcc, exec, s[18:19]
	v_cmp_ne_u32_e64 s[12:13], 1, v1
	v_readlane_b32 s45, v233, 1
	v_readlane_b32 s46, v233, 2
	v_readlane_b32 s47, v233, 3
	s_mov_b64 s[22:23], s[50:51]
	s_mov_b64 s[24:25], s[52:53]
	s_mov_b64 s[26:27], s[54:55]
	s_mov_b64 s[28:29], s[56:57]
	s_mov_b64 s[30:31], s[58:59]
	s_cbranch_vccnz .LBB0_2431
	s_and_b64 vcc, exec, s[12:13]
	s_cbranch_vccnz .LBB0_2430
	v_lshlrev_b32_e32 v3, 2, v130
	v_lshlrev_b32_e32 v2, 4, v130
	v_xor_b32_e32 v1, 64, v3
	v_xor_b32_e32 v126, 0x80, v3
	v_mov_b32_e32 v3, 0
	s_add_u32 s8, s6, 0x3b400000
	v_lshl_add_u64 v[4:5], s[16:17], 0, v[2:3]
	v_or_b32_e32 v6, 0x1000, v2
	v_or_b32_e32 v8, 0x1400, v2
	v_or_b32_e32 v10, 0x1800, v2
	v_or_b32_e32 v2, 0x1c00, v2
	s_addc_u32 s9, s7, 0
	v_lshl_add_u64 v[12:13], s[16:17], 0, v[2:3]
	v_lshlrev_b32_e32 v2, 3, v130
	s_add_u32 s10, s6, 0x3b500000
	v_lshl_add_u64 v[16:17], s[6:7], 0, v[2:3]
	s_mov_b64 s[0:1], 0x26c00000
	s_addc_u32 s11, s7, 0
	v_lshl_add_u64 v[14:15], v[16:17], 0, s[0:1]
	s_mov_b64 s[0:1], 0xe400000
	s_ashr_i32 s5, s4, 31
	s_lshl_b32 s18, s90, 4
	v_lshl_add_u64 v[16:17], v[16:17], 0, s[0:1]
	s_lshl_b64 s[0:1], s[4:5], 12
	s_add_u32 s20, s6, s0
	s_addc_u32 s21, s7, s1
	s_add_i32 s0, s4, s94
	s_ashr_i32 s19, s18, 31
	s_ashr_i32 s1, s0, 31
	s_lshl_b64 s[22:23], s[18:19], 12
	s_lshl_b64 s[0:1], s[0:1], 12
	s_add_u32 s24, s6, s0
	v_mov_b32_e32 v7, v3
	v_mov_b32_e32 v9, v3
	v_mov_b32_e32 v11, v3
	s_addc_u32 s25, s7, s1
	s_lshl_b32 s0, s96, 4
	s_lshl_b32 s1, s40, 1
	v_lshl_add_u64 v[6:7], s[16:17], 0, v[6:7]
	v_lshl_add_u64 v[8:9], s[16:17], 0, v[8:9]
	v_lshl_add_u64 v[10:11], s[16:17], 0, v[10:11]
	s_add_i32 s26, s0, s1
	s_lshl_b32 s5, s90, 5
	s_add_i32 s19, 0, 0x20080
	s_movk_i32 s28, 0x7fff
	v_mov_b32_e32 v127, 0x358637bd
	s_mov_b32 s29, 0xf800000
	v_mov_b32_e32 v128, 0x260
	s_mov_b32 s30, 0x16400000
	v_mov_b32_e32 v129, 1
	s_mov_b32 s31, s4
	global_load_dwordx4 v[166:169], v[4:5], off
	global_load_dwordx4 v[170:173], v[4:5], off offset:1024
	global_load_dwordx4 v[174:177], v[4:5], off offset:2048
	global_load_dwordx4 v[178:181], v[4:5], off offset:3072
	global_load_dwordx4 v[182:185], v[6:7], off
	global_load_dwordx4 v[186:189], v[8:9], off
	global_load_dwordx4 v[190:193], v[10:11], off
	global_load_dwordx4 v[194:197], v[12:13], off
	s_waitcnt vmcnt(0)
	s_branch .LBB0_2412

.LBB0_2428:
	v_mov_b64_e32 v[54:55], v[166:167]
	v_mov_b64_e32 v[56:57], v[168:169]
	v_and_b32_e32 v45, 0xffff0000, v120
	v_and_b32_e32 v44, 0xffff0000, v121
	v_pk_mul_f32 v[38:39], v[22:23], v[22:23]
	v_and_b32_e32 v73, 0xffff0000, v118
	v_pk_fma_f32 v[48:49], v[44:45], v[44:45], v[38:39]
	v_and_b32_e32 v72, 0xffff0000, v119
	v_pk_mul_f32 v[38:39], v[24:25], v[24:25]
	v_and_b32_e32 v85, 0xffff0000, v112
	v_pk_fma_f32 v[80:81], v[72:73], v[72:73], v[38:39]
	v_and_b32_e32 v84, 0xffff0000, v113
	v_pk_mul_f32 v[38:39], v[96:97], v[96:97]
	v_and_b32_e32 v43, 0xffff0000, v108
	v_pk_fma_f32 v[82:83], v[84:85], v[84:85], v[38:39]
	v_and_b32_e32 v42, 0xffff0000, v109
	v_pk_mul_f32 v[38:39], v[106:107], v[106:107]
	v_add_f32_e32 v52, v80, v81
	v_add_f32_e32 v48, v48, v49
	v_pk_fma_f32 v[88:89], v[42:43], v[42:43], v[38:39]
	v_and_b32_e32 v41, 0xffff0000, v104
	v_and_b32_e32 v40, 0xffff0000, v105
	v_pk_mul_f32 v[38:39], v[94:95], v[94:95]
	v_add_f32_e32 v48, v48, v52
	v_add_f32_e32 v49, v82, v83
	v_pk_fma_f32 v[92:93], v[40:41], v[40:41], v[38:39]
	v_and_b32_e32 v39, 0xffff0000, v114
	v_and_b32_e32 v38, 0xffff0000, v115
	v_pk_mul_f32 v[50:51], v[86:87], v[86:87]
	v_add_f32_e32 v48, v48, v49
	v_add_f32_e32 v49, v88, v89
	v_pk_fma_f32 v[98:99], v[38:39], v[38:39], v[50:51]
	v_and_b32_e32 v101, 0xffff0000, v102
	v_and_b32_e32 v100, 0xffff0000, v103
	v_pk_mul_f32 v[50:51], v[78:79], v[78:79]
	v_add_f32_e32 v48, v48, v49
	v_add_f32_e32 v49, v92, v93
	v_pk_fma_f32 v[102:103], v[100:101], v[100:101], v[50:51]
	v_and_b32_e32 v51, 0xffff0000, v110
	v_and_b32_e32 v50, 0xffff0000, v111
	v_pk_mul_f32 v[104:105], v[74:75], v[74:75]
	v_add_f32_e32 v48, v48, v49
	v_add_f32_e32 v49, v98, v99
	v_pk_fma_f32 v[104:105], v[50:51], v[50:51], v[104:105]
	v_add_f32_e32 v48, v48, v49
	v_add_f32_e32 v49, v102, v103
	v_add_f32_e32 v48, v48, v49
	v_add_f32_e32 v49, v104, v105
	v_add_f32_e32 v48, v48, v49
	s_nop 1
	v_add_f32_dpp v48, v48, v48 quad_perm:[1,0,3,2] row_mask:0xf bank_mask:0xf bound_ctrl:1
	s_nop 1
	v_add_f32_dpp v48, v48, v48 quad_perm:[2,3,0,1] row_mask:0xf bank_mask:0xf bound_ctrl:1
	s_nop 1
	v_add_f32_dpp v48, v48, v48 row_ror:4 row_mask:0xf bank_mask:0xf bound_ctrl:1
	s_nop 1
	v_add_f32_dpp v48, v48, v48 row_ror:8 row_mask:0xf bank_mask:0xf bound_ctrl:1
	ds_bpermute_b32 v49, v1, v48
	s_waitcnt lgkmcnt(0)
	v_add_f32_e32 v48, v48, v49
	ds_bpermute_b32 v49, v126, v48
	s_waitcnt lgkmcnt(0)
	v_add_f32_e32 v48, v48, v49
	v_fmamk_f32 v48, v48, 0x3a000000, v127
	v_mul_f32_e32 v49, 0x4f800000, v48
	v_cmp_gt_f32_e32 vcc, s29, v48
	s_nop 1
	v_cndmask_b32_e32 v48, v48, v49, vcc
	v_sqrt_f32_e32 v49, v48
	s_nop 0
	v_add_u32_e32 v52, -1, v49
	v_fma_f32 v67, -v52, v49, v48
	v_cmp_ge_f32_e64 s[14:15], 0, v67
	v_add_u32_e32 v67, 1, v49
	s_nop 0
	v_cndmask_b32_e64 v52, v49, v52, s[14:15]
	v_fma_f32 v49, -v67, v49, v48
	v_cmp_lt_f32_e64 s[14:15], 0, v49
	s_nop 1
	v_cndmask_b32_e64 v49, v52, v67, s[14:15]
	v_mul_f32_e32 v52, 0x37800000, v49
	v_cndmask_b32_e32 v49, v49, v52, vcc
	v_cmp_class_f32_e32 vcc, v48, v128
	s_nop 1
	v_cndmask_b32_e32 v48, v49, v48, vcc
	v_div_scale_f32 v49, s[2:3], v48, v48, 1.0
	v_rcp_f32_e32 v52, v49
	s_nop 0
	v_fma_f32 v67, -v49, v52, 1.0
	v_fmac_f32_e32 v52, v67, v52
	v_div_scale_f32 v67, vcc, 1.0, v48, 1.0
	v_mul_f32_e32 v80, v67, v52
	v_fma_f32 v81, -v49, v80, v67
	v_fmac_f32_e32 v80, v81, v52
	v_fma_f32 v49, -v49, v80, v67
	v_div_fmas_f32 v49, v49, v52, v80
	v_div_fixup_f32 v52, v49, v48, 1.0
	v_pk_mul_f32 v[44:45], v[52:53], v[44:45] op_sel_hi:[0,1]
	s_waitcnt vmcnt(0)
	v_mov_b32_e32 v48, v54
	v_mov_b32_e32 v49, v56
	v_pk_mul_f32 v[44:45], v[48:49], v[44:45]
	v_pk_mul_f32 v[22:23], v[52:53], v[22:23] op_sel_hi:[0,1]
	v_mov_b32_e32 v56, v55
	v_pk_mul_f32 v[22:23], v[56:57], v[22:23]
	v_and_b32_sdwa v48, v45, v129 dst_sel:DWORD dst_unused:UNUSED_PAD src0_sel:WORD_1 src1_sel:DWORD
	v_and_b32_sdwa v49, v44, v129 dst_sel:DWORD dst_unused:UNUSED_PAD src0_sel:WORD_1 src1_sel:DWORD
	v_add3_u32 v44, v44, v49, s28
	v_add3_u32 v45, v45, v48, s28
	v_and_b32_sdwa v48, v23, v129 dst_sel:DWORD dst_unused:UNUSED_PAD src0_sel:WORD_1 src1_sel:DWORD
	v_and_b32_sdwa v49, v22, v129 dst_sel:DWORD dst_unused:UNUSED_PAD src0_sel:WORD_1 src1_sel:DWORD
	v_add3_u32 v23, v23, v48, s28
	v_add3_u32 v22, v22, v49, s28
	v_and_b32_e32 v23, 0xffff0000, v23
	v_and_b32_e32 v22, 0xffff0000, v22
	v_add_co_u32_e32 v54, vcc, s30, v18
	v_or_b32_sdwa v23, v23, v45 dst_sel:DWORD dst_unused:UNUSED_PAD src0_sel:DWORD src1_sel:WORD_1
	v_or_b32_sdwa v22, v22, v44 dst_sel:DWORD dst_unused:UNUSED_PAD src0_sel:DWORD src1_sel:WORD_1
	v_addc_co_u32_e32 v55, vcc, 0, v19, vcc
	global_store_dwordx2 v[54:55], v[22:23], off
	v_mov_b64_e32 v[80:81], v[170:171]
	v_mov_b64_e32 v[82:83], v[172:173]
	v_pk_mul_f32 v[22:23], v[52:53], v[24:25] op_sel_hi:[0,1]
	v_pk_mul_f32 v[18:19], v[52:53], v[72:73] op_sel_hi:[0,1]
	v_and_b32_e32 v57, 0xffff0000, v90
	v_and_b32_e32 v56, 0xffff0000, v91
	v_pk_mul_f32 v[72:73], v[36:37], v[36:37]
	s_and_b64 vcc, exec, s[0:1]
	v_mov_b32_e32 v25, v82
	v_mov_b32_e32 v82, v81
	v_mov_b32_e32 v24, v80
	v_pk_mul_f32 v[22:23], v[82:83], v[22:23]
	v_pk_mul_f32 v[18:19], v[24:25], v[18:19]
	v_and_b32_sdwa v44, v23, v129 dst_sel:DWORD dst_unused:UNUSED_PAD src0_sel:WORD_1 src1_sel:DWORD
	v_and_b32_sdwa v45, v22, v129 dst_sel:DWORD dst_unused:UNUSED_PAD src0_sel:WORD_1 src1_sel:DWORD
	v_and_b32_sdwa v24, v19, v129 dst_sel:DWORD dst_unused:UNUSED_PAD src0_sel:WORD_1 src1_sel:DWORD
	v_and_b32_sdwa v25, v18, v129 dst_sel:DWORD dst_unused:UNUSED_PAD src0_sel:WORD_1 src1_sel:DWORD
	v_add3_u32 v23, v23, v44, s28
	v_add3_u32 v22, v22, v45, s28
	v_add3_u32 v18, v18, v25, s28
	v_add3_u32 v19, v19, v24, s28
	v_and_b32_e32 v23, 0xffff0000, v23
	v_and_b32_e32 v22, 0xffff0000, v22
	v_or_b32_sdwa v19, v23, v19 dst_sel:DWORD dst_unused:UNUSED_PAD src0_sel:DWORD src1_sel:WORD_1
	v_or_b32_sdwa v18, v22, v18 dst_sel:DWORD dst_unused:UNUSED_PAD src0_sel:DWORD src1_sel:WORD_1
	global_store_dwordx2 v[54:55], v[18:19], off offset:512
	v_mov_b64_e32 v[22:23], v[174:175]
	v_mov_b64_e32 v[24:25], v[176:177]
	v_pk_mul_f32 v[44:45], v[52:53], v[96:97] op_sel_hi:[0,1]
	v_pk_mul_f32 v[18:19], v[52:53], v[84:85] op_sel_hi:[0,1]
	v_mov_b32_e32 v49, v24
	v_mov_b32_e32 v24, v23
	v_mov_b32_e32 v48, v22
	v_pk_mul_f32 v[22:23], v[24:25], v[44:45]
	v_pk_mul_f32 v[18:19], v[48:49], v[18:19]
	v_and_b32_sdwa v44, v23, v129 dst_sel:DWORD dst_unused:UNUSED_PAD src0_sel:WORD_1 src1_sel:DWORD
	v_and_b32_sdwa v45, v22, v129 dst_sel:DWORD dst_unused:UNUSED_PAD src0_sel:WORD_1 src1_sel:DWORD
	v_and_b32_sdwa v24, v19, v129 dst_sel:DWORD dst_unused:UNUSED_PAD src0_sel:WORD_1 src1_sel:DWORD
	v_and_b32_sdwa v25, v18, v129 dst_sel:DWORD dst_unused:UNUSED_PAD src0_sel:WORD_1 src1_sel:DWORD
	v_add3_u32 v23, v23, v44, s28
	v_add3_u32 v22, v22, v45, s28
	v_add3_u32 v18, v18, v25, s28
	v_add3_u32 v19, v19, v24, s28
	v_and_b32_e32 v23, 0xffff0000, v23
	v_and_b32_e32 v22, 0xffff0000, v22
	v_or_b32_sdwa v19, v23, v19 dst_sel:DWORD dst_unused:UNUSED_PAD src0_sel:DWORD src1_sel:WORD_1
	v_or_b32_sdwa v18, v22, v18 dst_sel:DWORD dst_unused:UNUSED_PAD src0_sel:DWORD src1_sel:WORD_1
	global_store_dwordx2 v[54:55], v[18:19], off offset:1024
	v_mov_b64_e32 v[22:23], v[178:179]
	v_mov_b64_e32 v[24:25], v[180:181]
	v_pk_mul_f32 v[18:19], v[52:53], v[42:43] op_sel_hi:[0,1]
	v_pk_mul_f32 v[42:43], v[52:53], v[106:107] op_sel_hi:[0,1]
	v_and_b32_e32 v49, 0xffff0000, v76
	v_and_b32_e32 v48, 0xffff0000, v77
	v_pk_mul_f32 v[76:77], v[26:27], v[26:27]
	v_mov_b32_e32 v45, v24
	v_mov_b32_e32 v24, v23
	v_mov_b32_e32 v44, v22
	v_pk_mul_f32 v[22:23], v[42:43], v[24:25]
	v_pk_mul_f32 v[18:19], v[18:19], v[44:45]
	v_and_b32_sdwa v42, v23, v129 dst_sel:DWORD dst_unused:UNUSED_PAD src0_sel:WORD_1 src1_sel:DWORD
	v_and_b32_sdwa v43, v22, v129 dst_sel:DWORD dst_unused:UNUSED_PAD src0_sel:WORD_1 src1_sel:DWORD
	v_and_b32_sdwa v24, v19, v129 dst_sel:DWORD dst_unused:UNUSED_PAD src0_sel:WORD_1 src1_sel:DWORD
	v_and_b32_sdwa v25, v18, v129 dst_sel:DWORD dst_unused:UNUSED_PAD src0_sel:WORD_1 src1_sel:DWORD
	v_add3_u32 v23, v23, v42, s28
	v_add3_u32 v22, v22, v43, s28
	v_add3_u32 v18, v18, v25, s28
	v_add3_u32 v19, v19, v24, s28
	v_and_b32_e32 v23, 0xffff0000, v23
	v_and_b32_e32 v22, 0xffff0000, v22
	v_or_b32_sdwa v19, v23, v19 dst_sel:DWORD dst_unused:UNUSED_PAD src0_sel:DWORD src1_sel:WORD_1
	v_or_b32_sdwa v18, v22, v18 dst_sel:DWORD dst_unused:UNUSED_PAD src0_sel:DWORD src1_sel:WORD_1
	global_store_dwordx2 v[54:55], v[18:19], off offset:1536
	v_mov_b64_e32 v[22:23], v[182:183]
	v_mov_b64_e32 v[24:25], v[184:185]
	v_pk_mul_f32 v[18:19], v[52:53], v[40:41] op_sel_hi:[0,1]
	v_pk_mul_f32 v[40:41], v[52:53], v[94:95] op_sel_hi:[0,1]
	v_and_b32_e32 v45, 0xffff0000, v70
	v_and_b32_e32 v44, 0xffff0000, v71
	v_pk_mul_f32 v[70:71], v[34:35], v[34:35]
	v_mov_b32_e32 v43, v24
	v_mov_b32_e32 v24, v23
	v_mov_b32_e32 v42, v22
	v_pk_mul_f32 v[22:23], v[40:41], v[24:25]
	v_pk_mul_f32 v[18:19], v[18:19], v[42:43]
	v_and_b32_sdwa v40, v23, v129 dst_sel:DWORD dst_unused:UNUSED_PAD src0_sel:WORD_1 src1_sel:DWORD
	v_and_b32_sdwa v41, v22, v129 dst_sel:DWORD dst_unused:UNUSED_PAD src0_sel:WORD_1 src1_sel:DWORD
	v_and_b32_sdwa v24, v19, v129 dst_sel:DWORD dst_unused:UNUSED_PAD src0_sel:WORD_1 src1_sel:DWORD
	v_and_b32_sdwa v25, v18, v129 dst_sel:DWORD dst_unused:UNUSED_PAD src0_sel:WORD_1 src1_sel:DWORD
	v_add3_u32 v23, v23, v40, s28
	v_add3_u32 v22, v22, v41, s28
	v_add3_u32 v18, v18, v25, s28
	v_add3_u32 v19, v19, v24, s28
	v_and_b32_e32 v23, 0xffff0000, v23
	v_and_b32_e32 v22, 0xffff0000, v22
	v_or_b32_sdwa v19, v23, v19 dst_sel:DWORD dst_unused:UNUSED_PAD src0_sel:DWORD src1_sel:WORD_1
	v_or_b32_sdwa v18, v22, v18 dst_sel:DWORD dst_unused:UNUSED_PAD src0_sel:DWORD src1_sel:WORD_1
	global_store_dwordx2 v[54:55], v[18:19], off offset:2048
	v_mov_b64_e32 v[22:23], v[186:187]
	v_mov_b64_e32 v[24:25], v[188:189]
	v_pk_mul_f32 v[18:19], v[52:53], v[38:39] op_sel_hi:[0,1]
	v_pk_mul_f32 v[38:39], v[52:53], v[86:87] op_sel_hi:[0,1]
	v_and_b32_e32 v43, 0xffff0000, v64
	v_and_b32_e32 v42, 0xffff0000, v65
	v_pk_mul_f32 v[64:65], v[32:33], v[32:33]
	v_pk_fma_f32 v[70:71], v[44:45], v[44:45], v[70:71]
	v_pk_fma_f32 v[64:65], v[42:43], v[42:43], v[64:65]
	v_mov_b32_e32 v41, v24
	v_mov_b32_e32 v24, v23
	v_mov_b32_e32 v40, v22
	v_pk_mul_f32 v[22:23], v[38:39], v[24:25]
	v_pk_mul_f32 v[18:19], v[18:19], v[40:41]
	v_and_b32_sdwa v38, v23, v129 dst_sel:DWORD dst_unused:UNUSED_PAD src0_sel:WORD_1 src1_sel:DWORD
	v_and_b32_sdwa v39, v22, v129 dst_sel:DWORD dst_unused:UNUSED_PAD src0_sel:WORD_1 src1_sel:DWORD
	v_and_b32_sdwa v24, v19, v129 dst_sel:DWORD dst_unused:UNUSED_PAD src0_sel:WORD_1 src1_sel:DWORD
	v_and_b32_sdwa v25, v18, v129 dst_sel:DWORD dst_unused:UNUSED_PAD src0_sel:WORD_1 src1_sel:DWORD
	v_add3_u32 v23, v23, v38, s28
	v_add3_u32 v22, v22, v39, s28
	v_add3_u32 v18, v18, v25, s28
	v_add3_u32 v19, v19, v24, s28
	v_and_b32_e32 v23, 0xffff0000, v23
	v_and_b32_e32 v22, 0xffff0000, v22
	v_or_b32_sdwa v19, v23, v19 dst_sel:DWORD dst_unused:UNUSED_PAD src0_sel:DWORD src1_sel:WORD_1
	v_or_b32_sdwa v18, v22, v18 dst_sel:DWORD dst_unused:UNUSED_PAD src0_sel:DWORD src1_sel:WORD_1
	global_store_dwordx2 v[54:55], v[18:19], off offset:2560
	v_mov_b64_e32 v[22:23], v[190:191]
	v_mov_b64_e32 v[24:25], v[192:193]
	v_pk_mul_f32 v[38:39], v[52:53], v[78:79] op_sel_hi:[0,1]
	v_pk_mul_f32 v[18:19], v[52:53], v[100:101] op_sel_hi:[0,1]
	v_add_f32_e32 v64, v64, v65
	v_mov_b32_e32 v41, v24
	v_mov_b32_e32 v24, v23
	v_mov_b32_e32 v40, v22
	v_pk_mul_f32 v[22:23], v[38:39], v[24:25]
	v_pk_mul_f32 v[18:19], v[18:19], v[40:41]
	v_and_b32_sdwa v38, v23, v129 dst_sel:DWORD dst_unused:UNUSED_PAD src0_sel:WORD_1 src1_sel:DWORD
	v_and_b32_sdwa v39, v22, v129 dst_sel:DWORD dst_unused:UNUSED_PAD src0_sel:WORD_1 src1_sel:DWORD
	v_and_b32_sdwa v24, v19, v129 dst_sel:DWORD dst_unused:UNUSED_PAD src0_sel:WORD_1 src1_sel:DWORD
	v_and_b32_sdwa v25, v18, v129 dst_sel:DWORD dst_unused:UNUSED_PAD src0_sel:WORD_1 src1_sel:DWORD
	v_add3_u32 v23, v23, v38, s28
	v_add3_u32 v22, v22, v39, s28
	v_add3_u32 v18, v18, v25, s28
	v_add3_u32 v19, v19, v24, s28
	v_and_b32_e32 v23, 0xffff0000, v23
	v_and_b32_e32 v22, 0xffff0000, v22
	v_or_b32_sdwa v19, v23, v19 dst_sel:DWORD dst_unused:UNUSED_PAD src0_sel:DWORD src1_sel:WORD_1
	v_or_b32_sdwa v18, v22, v18 dst_sel:DWORD dst_unused:UNUSED_PAD src0_sel:DWORD src1_sel:WORD_1
	global_store_dwordx2 v[54:55], v[18:19], off offset:3072
	v_mov_b64_e32 v[78:79], v[194:195]
	v_mov_b64_e32 v[80:81], v[196:197]
	v_pk_mul_f32 v[24:25], v[68:69], v[68:69]
	v_and_b32_e32 v18, 0xffff0000, v66
	v_pk_fma_f32 v[24:25], v[56:57], v[56:57], v[24:25]
	v_pk_fma_f32 v[66:67], v[48:49], v[48:49], v[72:73]
	v_and_b32_e32 v23, 0xffff0000, v53
	v_add_f32_e32 v53, v66, v67
	v_add_f32_e32 v24, v24, v25
	v_and_b32_e32 v41, 0xffff0000, v58
	v_and_b32_e32 v40, 0xffff0000, v59
	v_pk_mul_f32 v[58:59], v[30:31], v[30:31]
	v_add_f32_e32 v25, v70, v71
	v_add_f32_e32 v24, v24, v53
	v_and_b32_e32 v39, 0xffff0000, v60
	v_and_b32_e32 v38, 0xffff0000, v61
	v_pk_mul_f32 v[60:61], v[28:29], v[28:29]
	v_pk_fma_f32 v[58:59], v[40:41], v[40:41], v[58:59]
	v_add_f32_e32 v24, v24, v25
	v_and_b32_e32 v22, 0xffff0000, v62
	v_pk_fma_f32 v[60:61], v[38:39], v[38:39], v[60:61]
	v_add_f32_e32 v58, v58, v59
	v_add_f32_e32 v24, v24, v64
	v_and_b32_e32 v19, 0xffff0000, v63
	v_pk_mul_f32 v[62:63], v[20:21], v[20:21]
	v_pk_fma_f32 v[72:73], v[22:23], v[22:23], v[76:77]
	v_add_f32_e32 v59, v60, v61
	v_add_f32_e32 v24, v24, v58
	v_pk_fma_f32 v[62:63], v[18:19], v[18:19], v[62:63]
	v_add_f32_e32 v60, v72, v73
	v_add_f32_e32 v24, v24, v59
	v_add_f32_e32 v61, v62, v63
	v_add_f32_e32 v24, v24, v60
	v_add_f32_e32 v24, v24, v61
	v_pk_mul_f32 v[50:51], v[52:53], v[50:51] op_sel_hi:[0,1]
	v_pk_mul_f32 v[52:53], v[52:53], v[74:75] op_sel_hi:[0,1]
	v_add_f32_dpp v24, v24, v24 quad_perm:[1,0,3,2] row_mask:0xf bank_mask:0xf bound_ctrl:1
	v_mov_b32_e32 v59, v80
	v_add_f32_dpp v24, v24, v24 quad_perm:[2,3,0,1] row_mask:0xf bank_mask:0xf bound_ctrl:1
	v_mov_b32_e32 v80, v79
	v_mov_b32_e32 v58, v78
	v_add_f32_dpp v24, v24, v24 row_ror:4 row_mask:0xf bank_mask:0xf bound_ctrl:1
	v_pk_mul_f32 v[52:53], v[52:53], v[80:81]
	v_pk_mul_f32 v[50:51], v[50:51], v[58:59]
	v_add_f32_dpp v24, v24, v24 row_ror:8 row_mask:0xf bank_mask:0xf bound_ctrl:1
	ds_bpermute_b32 v25, v1, v24
	v_and_b32_sdwa v60, v53, v129 dst_sel:DWORD dst_unused:UNUSED_PAD src0_sel:WORD_1 src1_sel:DWORD
	v_and_b32_sdwa v61, v52, v129 dst_sel:DWORD dst_unused:UNUSED_PAD src0_sel:WORD_1 src1_sel:DWORD
	v_and_b32_sdwa v58, v51, v129 dst_sel:DWORD dst_unused:UNUSED_PAD src0_sel:WORD_1 src1_sel:DWORD
	v_and_b32_sdwa v59, v50, v129 dst_sel:DWORD dst_unused:UNUSED_PAD src0_sel:WORD_1 src1_sel:DWORD
	s_waitcnt lgkmcnt(0)
	v_add_f32_e32 v24, v24, v25
	ds_bpermute_b32 v25, v126, v24
	v_add3_u32 v53, v53, v60, s28
	v_add3_u32 v52, v52, v61, s28
	v_add3_u32 v50, v50, v59, s28
	v_add3_u32 v51, v51, v58, s28
	v_and_b32_e32 v53, 0xffff0000, v53
	v_and_b32_e32 v52, 0xffff0000, v52
	v_or_b32_sdwa v51, v53, v51 dst_sel:DWORD dst_unused:UNUSED_PAD src0_sel:DWORD src1_sel:WORD_1
	v_or_b32_sdwa v50, v52, v50 dst_sel:DWORD dst_unused:UNUSED_PAD src0_sel:DWORD src1_sel:WORD_1
	global_store_dwordx2 v[54:55], v[50:51], off offset:3584
	s_cbranch_vccnz .LBB0_2411
	s_waitcnt lgkmcnt(0)
	v_add_f32_e32 v24, v24, v25
	v_fmamk_f32 v24, v24, 0x3a000000, v127
	v_cmp_gt_f32_e32 vcc, s29, v24
	v_mul_f32_e32 v25, 0x4f800000, v24
	s_nop 0
	v_cndmask_b32_e32 v24, v24, v25, vcc
	v_sqrt_f32_e32 v25, v24
	s_nop 0
	v_add_u32_e32 v50, -1, v25
	v_fma_f32 v51, -v50, v25, v24
	v_cmp_ge_f32_e64 s[0:1], 0, v51
	v_add_u32_e32 v51, 1, v25
	s_nop 0
	v_cndmask_b32_e64 v50, v25, v50, s[0:1]
	v_fma_f32 v25, -v51, v25, v24
	v_cmp_lt_f32_e64 s[0:1], 0, v25
	s_nop 1
	v_cndmask_b32_e64 v25, v50, v51, s[0:1]
	v_mul_f32_e32 v50, 0x37800000, v25
	v_cndmask_b32_e32 v25, v25, v50, vcc
	v_cmp_class_f32_e32 vcc, v24, v128
	s_nop 1
	v_cndmask_b32_e32 v24, v25, v24, vcc
	v_div_scale_f32 v25, s[0:1], v24, v24, 1.0
	v_rcp_f32_e32 v50, v25
	s_nop 0
	v_fma_f32 v51, -v25, v50, 1.0
	v_fmac_f32_e32 v50, v51, v50
	v_div_scale_f32 v51, vcc, 1.0, v24, 1.0
	v_mul_f32_e32 v52, v51, v50
	v_fma_f32 v53, -v25, v52, v51
	v_fmac_f32_e32 v52, v53, v50
	v_fma_f32 v25, -v25, v52, v51
	v_div_fmas_f32 v25, v25, v50, v52
	v_mov_b64_e32 v[50:51], v[166:167]
	v_mov_b64_e32 v[52:53], v[168:169]
	v_div_fixup_f32 v24, v25, v24, 1.0
	v_pk_mul_f32 v[54:55], v[24:25], v[56:57] op_sel_hi:[0,1]
	v_add_co_u32_e32 v46, vcc, s30, v46
	v_mov_b32_e32 v56, v50
	v_mov_b32_e32 v57, v52
	v_pk_mul_f32 v[54:55], v[54:55], v[56:57]
	v_pk_mul_f32 v[56:57], v[24:25], v[68:69] op_sel_hi:[0,1]
	v_mov_b32_e32 v52, v51
	v_pk_mul_f32 v[50:51], v[56:57], v[52:53]
	v_and_b32_sdwa v52, v54, v129 dst_sel:DWORD dst_unused:UNUSED_PAD src0_sel:WORD_1 src1_sel:DWORD
	v_add3_u32 v52, v54, v52, s28
	v_and_b32_sdwa v53, v51, v129 dst_sel:DWORD dst_unused:UNUSED_PAD src0_sel:WORD_1 src1_sel:DWORD
	v_and_b32_sdwa v54, v50, v129 dst_sel:DWORD dst_unused:UNUSED_PAD src0_sel:WORD_1 src1_sel:DWORD
	v_and_b32_sdwa v25, v55, v129 dst_sel:DWORD dst_unused:UNUSED_PAD src0_sel:WORD_1 src1_sel:DWORD
	v_add3_u32 v51, v51, v53, s28
	v_add3_u32 v50, v50, v54, s28
	v_add3_u32 v25, v55, v25, s28
	v_and_b32_e32 v51, 0xffff0000, v51
	v_and_b32_e32 v50, 0xffff0000, v50
	v_or_b32_sdwa v51, v51, v25 dst_sel:DWORD dst_unused:UNUSED_PAD src0_sel:DWORD src1_sel:WORD_1
	v_or_b32_sdwa v50, v50, v52 dst_sel:DWORD dst_unused:UNUSED_PAD src0_sel:DWORD src1_sel:WORD_1
	v_addc_co_u32_e32 v47, vcc, 0, v47, vcc
	global_store_dwordx2 v[46:47], v[50:51], off
	v_mov_b64_e32 v[50:51], v[170:171]
	v_mov_b64_e32 v[52:53], v[172:173]
	v_pk_mul_f32 v[48:49], v[24:25], v[48:49] op_sel_hi:[0,1]
	v_pk_mul_f32 v[36:37], v[24:25], v[36:37] op_sel_hi:[0,1]
	v_mov_b32_e32 v54, v50
	v_mov_b32_e32 v55, v52
	v_pk_mul_f32 v[48:49], v[48:49], v[54:55]
	v_mov_b32_e32 v52, v51
	v_pk_mul_f32 v[36:37], v[36:37], v[52:53]
	v_and_b32_sdwa v25, v49, v129 dst_sel:DWORD dst_unused:UNUSED_PAD src0_sel:WORD_1 src1_sel:DWORD
	v_and_b32_sdwa v50, v48, v129 dst_sel:DWORD dst_unused:UNUSED_PAD src0_sel:WORD_1 src1_sel:DWORD
	v_add3_u32 v48, v48, v50, s28
	v_add3_u32 v25, v49, v25, s28
	v_and_b32_sdwa v49, v37, v129 dst_sel:DWORD dst_unused:UNUSED_PAD src0_sel:WORD_1 src1_sel:DWORD
	v_and_b32_sdwa v50, v36, v129 dst_sel:DWORD dst_unused:UNUSED_PAD src0_sel:WORD_1 src1_sel:DWORD
	v_add3_u32 v37, v37, v49, s28
	v_add3_u32 v36, v36, v50, s28
	v_and_b32_e32 v37, 0xffff0000, v37
	v_and_b32_e32 v36, 0xffff0000, v36
	v_or_b32_sdwa v37, v37, v25 dst_sel:DWORD dst_unused:UNUSED_PAD src0_sel:DWORD src1_sel:WORD_1
	v_or_b32_sdwa v36, v36, v48 dst_sel:DWORD dst_unused:UNUSED_PAD src0_sel:DWORD src1_sel:WORD_1
	global_store_dwordx2 v[46:47], v[36:37], off offset:512
	v_mov_b64_e32 v[48:49], v[174:175]
	v_mov_b64_e32 v[50:51], v[176:177]
	v_pk_mul_f32 v[36:37], v[24:25], v[44:45] op_sel_hi:[0,1]
	v_pk_mul_f32 v[34:35], v[24:25], v[34:35] op_sel_hi:[0,1]
	v_mov_b32_e32 v44, v48
	v_mov_b32_e32 v45, v50
	v_pk_mul_f32 v[36:37], v[36:37], v[44:45]
	v_mov_b32_e32 v50, v49
	v_pk_mul_f32 v[34:35], v[34:35], v[50:51]
	v_and_b32_sdwa v25, v37, v129 dst_sel:DWORD dst_unused:UNUSED_PAD src0_sel:WORD_1 src1_sel:DWORD
	v_and_b32_sdwa v44, v36, v129 dst_sel:DWORD dst_unused:UNUSED_PAD src0_sel:WORD_1 src1_sel:DWORD
	v_add3_u32 v36, v36, v44, s28
	v_add3_u32 v25, v37, v25, s28
	v_and_b32_sdwa v37, v35, v129 dst_sel:DWORD dst_unused:UNUSED_PAD src0_sel:WORD_1 src1_sel:DWORD
	v_and_b32_sdwa v44, v34, v129 dst_sel:DWORD dst_unused:UNUSED_PAD src0_sel:WORD_1 src1_sel:DWORD
	v_add3_u32 v35, v35, v37, s28
	v_add3_u32 v34, v34, v44, s28
	v_and_b32_e32 v35, 0xffff0000, v35
	v_and_b32_e32 v34, 0xffff0000, v34
	v_or_b32_sdwa v35, v35, v25 dst_sel:DWORD dst_unused:UNUSED_PAD src0_sel:DWORD src1_sel:WORD_1
	v_or_b32_sdwa v34, v34, v36 dst_sel:DWORD dst_unused:UNUSED_PAD src0_sel:DWORD src1_sel:WORD_1
	global_store_dwordx2 v[46:47], v[34:35], off offset:1024
	v_mov_b64_e32 v[34:35], v[178:179]
	v_mov_b64_e32 v[36:37], v[180:181]
	v_pk_mul_f32 v[32:33], v[24:25], v[32:33] op_sel_hi:[0,1]
	v_pk_mul_f32 v[42:43], v[24:25], v[42:43] op_sel_hi:[0,1]
	v_mov_b32_e32 v45, v36
	v_mov_b32_e32 v36, v35
	v_mov_b32_e32 v44, v34
	v_pk_mul_f32 v[32:33], v[32:33], v[36:37]
	v_pk_mul_f32 v[42:43], v[42:43], v[44:45]
	v_and_b32_sdwa v35, v33, v129 dst_sel:DWORD dst_unused:UNUSED_PAD src0_sel:WORD_1 src1_sel:DWORD
	v_and_b32_sdwa v36, v32, v129 dst_sel:DWORD dst_unused:UNUSED_PAD src0_sel:WORD_1 src1_sel:DWORD
	v_and_b32_sdwa v25, v43, v129 dst_sel:DWORD dst_unused:UNUSED_PAD src0_sel:WORD_1 src1_sel:DWORD
	v_and_b32_sdwa v34, v42, v129 dst_sel:DWORD dst_unused:UNUSED_PAD src0_sel:WORD_1 src1_sel:DWORD
	v_add3_u32 v33, v33, v35, s28
	v_add3_u32 v32, v32, v36, s28
	v_add3_u32 v34, v42, v34, s28
	v_add3_u32 v25, v43, v25, s28
	v_and_b32_e32 v33, 0xffff0000, v33
	v_and_b32_e32 v32, 0xffff0000, v32
	v_or_b32_sdwa v33, v33, v25 dst_sel:DWORD dst_unused:UNUSED_PAD src0_sel:DWORD src1_sel:WORD_1
	v_or_b32_sdwa v32, v32, v34 dst_sel:DWORD dst_unused:UNUSED_PAD src0_sel:DWORD src1_sel:WORD_1
	global_store_dwordx2 v[46:47], v[32:33], off offset:1536
	v_mov_b64_e32 v[32:33], v[182:183]
	v_mov_b64_e32 v[34:35], v[184:185]
	v_pk_mul_f32 v[36:37], v[24:25], v[40:41] op_sel_hi:[0,1]
	v_pk_mul_f32 v[30:31], v[24:25], v[30:31] op_sel_hi:[0,1]
	v_mov_b32_e32 v41, v34
	v_mov_b32_e32 v34, v33
	v_mov_b32_e32 v40, v32
	v_pk_mul_f32 v[30:31], v[30:31], v[34:35]
	v_pk_mul_f32 v[36:37], v[36:37], v[40:41]
	v_and_b32_sdwa v33, v31, v129 dst_sel:DWORD dst_unused:UNUSED_PAD src0_sel:WORD_1 src1_sel:DWORD
	v_and_b32_sdwa v34, v30, v129 dst_sel:DWORD dst_unused:UNUSED_PAD src0_sel:WORD_1 src1_sel:DWORD
	v_and_b32_sdwa v25, v37, v129 dst_sel:DWORD dst_unused:UNUSED_PAD src0_sel:WORD_1 src1_sel:DWORD
	v_and_b32_sdwa v32, v36, v129 dst_sel:DWORD dst_unused:UNUSED_PAD src0_sel:WORD_1 src1_sel:DWORD
	v_add3_u32 v31, v31, v33, s28
	v_add3_u32 v30, v30, v34, s28
	v_add3_u32 v32, v36, v32, s28
	v_add3_u32 v25, v37, v25, s28
	v_and_b32_e32 v31, 0xffff0000, v31
	v_and_b32_e32 v30, 0xffff0000, v30
	v_or_b32_sdwa v31, v31, v25 dst_sel:DWORD dst_unused:UNUSED_PAD src0_sel:DWORD src1_sel:WORD_1
	v_or_b32_sdwa v30, v30, v32 dst_sel:DWORD dst_unused:UNUSED_PAD src0_sel:DWORD src1_sel:WORD_1
	global_store_dwordx2 v[46:47], v[30:31], off offset:2048
	v_mov_b64_e32 v[30:31], v[186:187]
	v_mov_b64_e32 v[32:33], v[188:189]
	v_pk_mul_f32 v[28:29], v[24:25], v[28:29] op_sel_hi:[0,1]
	v_pk_mul_f32 v[34:35], v[24:25], v[38:39] op_sel_hi:[0,1]
	v_mov_b32_e32 v37, v32
	v_mov_b32_e32 v32, v31
	v_mov_b32_e32 v36, v30
	v_pk_mul_f32 v[28:29], v[28:29], v[32:33]
	v_pk_mul_f32 v[34:35], v[34:35], v[36:37]
	v_and_b32_sdwa v31, v29, v129 dst_sel:DWORD dst_unused:UNUSED_PAD src0_sel:WORD_1 src1_sel:DWORD
	v_and_b32_sdwa v32, v28, v129 dst_sel:DWORD dst_unused:UNUSED_PAD src0_sel:WORD_1 src1_sel:DWORD
	v_and_b32_sdwa v25, v35, v129 dst_sel:DWORD dst_unused:UNUSED_PAD src0_sel:WORD_1 src1_sel:DWORD
	v_and_b32_sdwa v30, v34, v129 dst_sel:DWORD dst_unused:UNUSED_PAD src0_sel:WORD_1 src1_sel:DWORD
	v_add3_u32 v29, v29, v31, s28
	v_add3_u32 v28, v28, v32, s28
	v_add3_u32 v30, v34, v30, s28
	v_add3_u32 v25, v35, v25, s28
	v_and_b32_e32 v29, 0xffff0000, v29
	v_and_b32_e32 v28, 0xffff0000, v28
	v_or_b32_sdwa v29, v29, v25 dst_sel:DWORD dst_unused:UNUSED_PAD src0_sel:DWORD src1_sel:WORD_1
	v_or_b32_sdwa v28, v28, v30 dst_sel:DWORD dst_unused:UNUSED_PAD src0_sel:DWORD src1_sel:WORD_1
	global_store_dwordx2 v[46:47], v[28:29], off offset:2560
	v_mov_b64_e32 v[28:29], v[190:191]
	v_mov_b64_e32 v[30:31], v[192:193]
	v_pk_mul_f32 v[22:23], v[24:25], v[22:23] op_sel_hi:[0,1]
	v_pk_mul_f32 v[26:27], v[24:25], v[26:27] op_sel_hi:[0,1]
	v_mov_b32_e32 v32, v28
	v_mov_b32_e32 v33, v30
	v_pk_mul_f32 v[22:23], v[22:23], v[32:33]
	v_mov_b32_e32 v30, v29
	v_pk_mul_f32 v[26:27], v[26:27], v[30:31]
	v_and_b32_sdwa v25, v23, v129 dst_sel:DWORD dst_unused:UNUSED_PAD src0_sel:WORD_1 src1_sel:DWORD
	v_and_b32_sdwa v28, v22, v129 dst_sel:DWORD dst_unused:UNUSED_PAD src0_sel:WORD_1 src1_sel:DWORD
	v_add3_u32 v22, v22, v28, s28
	v_add3_u32 v23, v23, v25, s28
	v_and_b32_sdwa v25, v27, v129 dst_sel:DWORD dst_unused:UNUSED_PAD src0_sel:WORD_1 src1_sel:DWORD
	v_and_b32_sdwa v28, v26, v129 dst_sel:DWORD dst_unused:UNUSED_PAD src0_sel:WORD_1 src1_sel:DWORD
	v_add3_u32 v25, v27, v25, s28
	v_add3_u32 v26, v26, v28, s28
	v_and_b32_e32 v25, 0xffff0000, v25
	v_and_b32_e32 v26, 0xffff0000, v26
	v_or_b32_sdwa v23, v25, v23 dst_sel:DWORD dst_unused:UNUSED_PAD src0_sel:DWORD src1_sel:WORD_1
	v_or_b32_sdwa v22, v26, v22 dst_sel:DWORD dst_unused:UNUSED_PAD src0_sel:DWORD src1_sel:WORD_1
	global_store_dwordx2 v[46:47], v[22:23], off offset:3072
	v_mov_b64_e32 v[26:27], v[194:195]
	v_mov_b64_e32 v[28:29], v[196:197]
	v_pk_mul_f32 v[18:19], v[24:25], v[18:19] op_sel_hi:[0,1]
	v_pk_mul_f32 v[20:21], v[24:25], v[20:21] op_sel_hi:[0,1]
	v_mov_b32_e32 v22, v26
	v_mov_b32_e32 v23, v28
	v_pk_mul_f32 v[18:19], v[18:19], v[22:23]
	v_mov_b32_e32 v28, v27
	v_pk_mul_f32 v[20:21], v[20:21], v[28:29]
	v_and_b32_sdwa v22, v19, v129 dst_sel:DWORD dst_unused:UNUSED_PAD src0_sel:WORD_1 src1_sel:DWORD
	v_and_b32_sdwa v23, v18, v129 dst_sel:DWORD dst_unused:UNUSED_PAD src0_sel:WORD_1 src1_sel:DWORD
	v_add3_u32 v18, v18, v23, s28
	v_add3_u32 v19, v19, v22, s28
	v_and_b32_sdwa v22, v21, v129 dst_sel:DWORD dst_unused:UNUSED_PAD src0_sel:WORD_1 src1_sel:DWORD
	v_and_b32_sdwa v23, v20, v129 dst_sel:DWORD dst_unused:UNUSED_PAD src0_sel:WORD_1 src1_sel:DWORD
	v_add3_u32 v21, v21, v22, s28
	v_add3_u32 v20, v20, v23, s28
	v_and_b32_e32 v21, 0xffff0000, v21
	v_and_b32_e32 v20, 0xffff0000, v20
	v_or_b32_sdwa v19, v21, v19 dst_sel:DWORD dst_unused:UNUSED_PAD src0_sel:DWORD src1_sel:WORD_1
	v_or_b32_sdwa v18, v20, v18 dst_sel:DWORD dst_unused:UNUSED_PAD src0_sel:DWORD src1_sel:WORD_1
	global_store_dwordx2 v[46:47], v[18:19], off offset:3584
	s_branch .LBB0_2411

.LBB0_4164:
	s_or_b64 exec, exec, s[16:17]
	s_andn2_b64 vcc, exec, s[14:15]
	s_mov_b32 s16, s24
	s_mov_b32 s17, s23
	s_waitcnt lgkmcnt(0)
	s_barrier
	s_cbranch_vccnz .LBB0_4118
	global_load_dwordx4 v[166:169], v[6:7], off
	global_load_dwordx4 v[170:173], v[6:7], off offset:1024
	global_load_dwordx4 v[174:177], v[6:7], off offset:2048
	global_load_dwordx4 v[178:181], v[6:7], off offset:3072
	global_load_dwordx4 v[182:185], v[8:9], off
	global_load_dwordx4 v[186:189], v[10:11], off
	global_load_dwordx4 v[190:193], v[12:13], off
	global_load_dwordx4 v[194:197], v[14:15], off
	s_waitcnt vmcnt(0)
.LBB0_4165:
	v_mov_b32_e32 v5, s16
	ds_read_b96 v[28:30], v5
	s_waitcnt lgkmcnt(0)
	v_readfirstlane_b32 s2, v28
	s_ashr_i32 s3, s2, 31
	s_lshl_b64 s[18:19], s[2:3], 2
	s_add_u32 s18, s20, s18
	s_addc_u32 s19, s21, s19
	s_lshl_b64 s[2:3], s[2:3], 12
	v_lshl_add_u64 v[20:21], v[16:17], 0, s[2:3]
	global_load_dword v28, v4, s[18:19]
	global_load_dwordx2 v[32:33], v[20:21], off
	v_mov_b64_e32 v[24:25], v[166:167]
	v_mov_b64_e32 v[26:27], v[168:169]
	v_ashrrev_i32_e32 v35, 31, v29
	v_mov_b32_e32 v34, v29
	v_ashrrev_i32_e32 v31, 31, v30
	v_lshlrev_b64 v[34:35], 12, v[34:35]
	v_lshlrev_b64 v[30:31], 12, v[30:31]
	v_lshl_add_u64 v[34:35], v[18:19], 0, v[34:35]
	v_lshl_add_u64 v[30:31], v[18:19], 0, v[30:31]
	global_load_dwordx2 v[36:37], v[20:21], off offset:512
	global_load_dwordx2 v[38:39], v[20:21], off offset:1024
	global_load_dwordx2 v[40:41], v[20:21], off offset:1536
	global_load_dwordx2 v[42:43], v[20:21], off offset:2048
	global_load_dwordx2 v[44:45], v[20:21], off offset:2560
	global_load_dwordx2 v[46:47], v[20:21], off offset:3072
	s_nop 0
	global_load_dwordx2 v[20:21], v[20:21], off offset:3584
	s_add_i32 s17, s17, 8
	s_addk_i32 s16, 0x80
	s_cmp_gt_i32 s17, 55
	s_waitcnt vmcnt(7)
	v_lshlrev_b32_e32 v48, 16, v32
	v_and_b32_e32 v49, 0xffff0000, v32
	v_lshlrev_b32_e32 v32, 16, v33
	v_and_b32_e32 v33, 0xffff0000, v33
	s_waitcnt vmcnt(7)
	v_pk_mul_f32 v[24:25], v[24:25], v[48:49]
	v_pk_mul_f32 v[26:27], v[26:27], v[32:33]
	v_pk_mul_f32 v[24:25], v[28:29], v[24:25] op_sel_hi:[0,1]
	v_pk_mul_f32 v[26:27], v[28:29], v[26:27] op_sel_hi:[0,1]
	v_cvt_pk_bf16_f32 v24, v24, v25
	v_cvt_pk_bf16_f32 v25, v26, v27
	global_store_dwordx2 v[34:35], v[24:25], off
	global_store_dwordx2 v[30:31], v[24:25], off
	v_mov_b64_e32 v[24:25], v[170:171]
	v_mov_b64_e32 v[26:27], v[172:173]
	s_waitcnt vmcnt(8)
	v_lshlrev_b32_e32 v32, 16, v36
	v_and_b32_e32 v33, 0xffff0000, v36
	v_lshlrev_b32_e32 v36, 16, v37
	v_and_b32_e32 v37, 0xffff0000, v37
	s_waitcnt vmcnt(0)
	v_pk_mul_f32 v[24:25], v[24:25], v[32:33]
	v_pk_mul_f32 v[26:27], v[26:27], v[36:37]
	v_pk_mul_f32 v[24:25], v[28:29], v[24:25] op_sel_hi:[0,1]
	v_pk_mul_f32 v[26:27], v[28:29], v[26:27] op_sel_hi:[0,1]
	v_cvt_pk_bf16_f32 v24, v24, v25
	v_cvt_pk_bf16_f32 v25, v26, v27
	global_store_dwordx2 v[34:35], v[24:25], off offset:512
	global_store_dwordx2 v[30:31], v[24:25], off offset:512
	v_mov_b64_e32 v[24:25], v[174:175]
	v_mov_b64_e32 v[26:27], v[176:177]
	v_lshlrev_b32_e32 v32, 16, v38
	v_and_b32_e32 v33, 0xffff0000, v38
	v_lshlrev_b32_e32 v36, 16, v39
	v_and_b32_e32 v37, 0xffff0000, v39
	v_pk_mul_f32 v[24:25], v[24:25], v[32:33]
	v_pk_mul_f32 v[26:27], v[26:27], v[36:37]
	v_pk_mul_f32 v[24:25], v[28:29], v[24:25] op_sel_hi:[0,1]
	v_pk_mul_f32 v[26:27], v[28:29], v[26:27] op_sel_hi:[0,1]
	v_cvt_pk_bf16_f32 v24, v24, v25
	v_cvt_pk_bf16_f32 v25, v26, v27
	global_store_dwordx2 v[34:35], v[24:25], off offset:1024
	global_store_dwordx2 v[30:31], v[24:25], off offset:1024
	v_mov_b64_e32 v[24:25], v[178:179]
	v_mov_b64_e32 v[26:27], v[180:181]
	v_lshlrev_b32_e32 v32, 16, v40
	v_and_b32_e32 v33, 0xffff0000, v40
	v_lshlrev_b32_e32 v36, 16, v41
	v_and_b32_e32 v37, 0xffff0000, v41
	v_pk_mul_f32 v[24:25], v[24:25], v[32:33]
	v_pk_mul_f32 v[26:27], v[26:27], v[36:37]
	v_pk_mul_f32 v[24:25], v[28:29], v[24:25] op_sel_hi:[0,1]
	v_pk_mul_f32 v[26:27], v[28:29], v[26:27] op_sel_hi:[0,1]
	v_cvt_pk_bf16_f32 v24, v24, v25
	v_cvt_pk_bf16_f32 v25, v26, v27
	global_store_dwordx2 v[34:35], v[24:25], off offset:1536
	global_store_dwordx2 v[30:31], v[24:25], off offset:1536
	v_mov_b64_e32 v[24:25], v[182:183]
	v_mov_b64_e32 v[26:27], v[184:185]
	v_lshlrev_b32_e32 v32, 16, v42
	v_and_b32_e32 v33, 0xffff0000, v42
	v_lshlrev_b32_e32 v36, 16, v43
	v_and_b32_e32 v37, 0xffff0000, v43
	v_pk_mul_f32 v[24:25], v[24:25], v[32:33]
	v_pk_mul_f32 v[26:27], v[26:27], v[36:37]
	v_pk_mul_f32 v[24:25], v[28:29], v[24:25] op_sel_hi:[0,1]
	v_pk_mul_f32 v[26:27], v[28:29], v[26:27] op_sel_hi:[0,1]
	v_cvt_pk_bf16_f32 v24, v24, v25
	v_cvt_pk_bf16_f32 v25, v26, v27
	global_store_dwordx2 v[34:35], v[24:25], off offset:2048
	global_store_dwordx2 v[30:31], v[24:25], off offset:2048
	v_mov_b64_e32 v[24:25], v[186:187]
	v_mov_b64_e32 v[26:27], v[188:189]
	v_lshlrev_b32_e32 v32, 16, v44
	v_and_b32_e32 v33, 0xffff0000, v44
	v_lshlrev_b32_e32 v36, 16, v45
	v_and_b32_e32 v37, 0xffff0000, v45
	v_pk_mul_f32 v[24:25], v[24:25], v[32:33]
	v_pk_mul_f32 v[26:27], v[26:27], v[36:37]
	v_pk_mul_f32 v[24:25], v[28:29], v[24:25] op_sel_hi:[0,1]
	v_pk_mul_f32 v[26:27], v[28:29], v[26:27] op_sel_hi:[0,1]
	v_cvt_pk_bf16_f32 v24, v24, v25
	v_cvt_pk_bf16_f32 v25, v26, v27
	global_store_dwordx2 v[34:35], v[24:25], off offset:2560
	global_store_dwordx2 v[30:31], v[24:25], off offset:2560
	v_mov_b64_e32 v[24:25], v[190:191]
	v_mov_b64_e32 v[26:27], v[192:193]
	v_lshlrev_b32_e32 v32, 16, v46
	v_and_b32_e32 v33, 0xffff0000, v46
	v_lshlrev_b32_e32 v36, 16, v47
	v_and_b32_e32 v37, 0xffff0000, v47
	v_pk_mul_f32 v[24:25], v[24:25], v[32:33]
	v_pk_mul_f32 v[26:27], v[26:27], v[36:37]
	v_pk_mul_f32 v[24:25], v[28:29], v[24:25] op_sel_hi:[0,1]
	v_pk_mul_f32 v[26:27], v[28:29], v[26:27] op_sel_hi:[0,1]
	v_cvt_pk_bf16_f32 v24, v24, v25
	v_cvt_pk_bf16_f32 v25, v26, v27
	global_store_dwordx2 v[34:35], v[24:25], off offset:3072
	global_store_dwordx2 v[30:31], v[24:25], off offset:3072
	v_mov_b64_e32 v[24:25], v[194:195]
	v_mov_b64_e32 v[26:27], v[196:197]
	v_lshlrev_b32_e32 v32, 16, v20
	v_and_b32_e32 v33, 0xffff0000, v20
	v_lshlrev_b32_e32 v20, 16, v21
	v_and_b32_e32 v21, 0xffff0000, v21
	v_pk_mul_f32 v[24:25], v[24:25], v[32:33]
	v_pk_mul_f32 v[20:21], v[26:27], v[20:21]
	v_pk_mul_f32 v[24:25], v[28:29], v[24:25] op_sel_hi:[0,1]
	v_pk_mul_f32 v[20:21], v[28:29], v[20:21] op_sel_hi:[0,1]
	v_cvt_pk_bf16_f32 v24, v24, v25
	v_cvt_pk_bf16_f32 v25, v20, v21
	global_store_dwordx2 v[34:35], v[24:25], off offset:3584
	global_store_dwordx2 v[30:31], v[24:25], off offset:3584
	s_cbranch_scc0 .LBB0_4165
	s_branch .LBB0_4118
